# P12: final_g staged in LDS so the per-row output stores no longer serialize behind load+vmcnt(0) round trips; P8 tiles: loop-invariant norm/mod vectors from LDS; DPP wave reductions; P6 x128 fp8 MFMA;
# speedup vs baseline: 1.0057x; 1.0057x over previous
; DI unsigned pk2(float lo, float hi) { f32x2 v = {lo, hi}; bf16x2_t b = __builtin_convertvector(v, bf16x2_t); return __builtin_bit_cast(unsigned, b); }
; DI float bflo(unsigned w) { return __uint_as_float(w << 16); }
; DI float bfhi(unsigned w) { return __uint_as_float(w & 0xffff0000u); }
; __global__ void __launch_bounds__(NWAVES * 64, 2) fwd_kernel(Args a_unused) {
;     ...
;         bf16x8 bh[8][2], bl[8][2];
; #pragma unroll
;         for (int sK = 0; sK < 8; ++sK)
; #pragma unroll
;             for (int eh = 0; eh < 2; ++eh) { u32x4 ph, pl;
; #pragma unroll
;                 for (int i2 = 0; i2 < 4; ++i2) { const float w0 = wrp[(256 * wave + 32 * sK + 8 * kk + 2 * i2) * 32 + 16 * eh + r16], w1 = wrp[(256 * wave + 32 * sK + 8 * kk + 2 * i2 + 1) * 32 + 16 * eh + r16];
;                     const unsigned h = pk2(w0, w1); ph[i2] = h; pl[i2] = pk2(w0 - bflo(h), w1 - bfhi(h)); }
;                 bh[sK][eh] = __builtin_bit_cast(bf16x8, ph); bl[sK][eh] = __builtin_bit_cast(bf16x8, pl); }
.LBB0_1860:
	s_cmpk_gt_i32 s97, 0x3ff
	s_cbranch_scc1 .LBB0_1959
	v_lshrrev_b32_e32 v130, 4, v162
	v_and_b32_e32 v1, 15, v0
	s_lshl_b32 s3, s96, 13
	s_waitcnt vmcnt(0)
	v_lshlrev_b32_e32 v2, 8, v130
	v_or3_b32 v2, s3, v2, v1
	v_ashrrev_i32_e32 v3, 31, v2
	s_waitcnt lgkmcnt(0)
	v_lshl_add_u64 v[84:85], v[2:3], 2, s[18:19]
	v_add_co_u32_e32 v4, vcc, 0x147000, v84
	s_mov_b32 s3, 0x146000
	s_nop 0
	v_addc_co_u32_e32 v5, vcc, 0, v85, vcc
	global_load_dword v8, v[4:5], off offset:576
	global_load_dword v9, v[4:5], off offset:704
	global_load_dword v10, v[4:5], off offset:832
	global_load_dword v11, v[4:5], off offset:960
	global_load_dword v12, v[4:5], off
	global_load_dword v14, v[4:5], off offset:64
	global_load_dword v15, v[4:5], off offset:192
	global_load_dword v16, v[4:5], off offset:320
	global_load_dword v17, v[4:5], off offset:448
	global_load_dword v18, v[4:5], off offset:512
	global_load_dword v21, v[4:5], off offset:384
	global_load_dword v20, v[4:5], off offset:256
	global_load_dword v13, v[4:5], off offset:128
	v_add_co_u32_e32 v2, vcc, s3, v84
	s_mov_b32 s3, 0x145000
	s_nop 0
	v_addc_co_u32_e32 v3, vcc, 0, v85, vcc
	global_load_dword v28, v[2:3], off
	global_load_dword v31, v[4:5], off offset:896
	global_load_dword v30, v[4:5], off offset:768
	global_load_dword v19, v[4:5], off offset:640
	global_load_dword v22, v[2:3], off offset:64
	global_load_dword v23, v[2:3], off offset:192
	global_load_dword v26, v[2:3], off offset:320
	global_load_dword v27, v[2:3], off offset:448
	global_load_dword v24, v[2:3], off offset:576
	global_load_dword v25, v[2:3], off offset:704
	global_load_dword v36, v[2:3], off offset:832
	global_load_dword v37, v[2:3], off offset:960
	s_mov_b64 s[4:5], 0x140000
	v_add_co_u32_e32 v38, vcc, s3, v84
	v_lshl_add_u64 v[96:97], v[84:85], 0, s[4:5]
	s_nop 0
	v_addc_co_u32_e32 v39, vcc, 0, v85, vcc
	global_load_dword v32, v[2:3], off offset:512
	global_load_dword v35, v[2:3], off offset:384
	global_load_dword v34, v[2:3], off offset:256
	global_load_dword v29, v[2:3], off offset:128
	global_load_dword v44, v[38:39], off
	global_load_dword v43, v[2:3], off offset:896
	global_load_dword v42, v[2:3], off offset:768
	global_load_dword v33, v[2:3], off offset:640
	global_load_dword v40, v[38:39], off offset:64
	global_load_dword v41, v[38:39], off offset:192
	global_load_dword v123, v[96:97], off offset:960
	s_mov_b32 s3, 0x144000
	s_lshl_b32 s30, s96, 1
	s_add_u32 s10, s18, 0x5fc00000
	v_mov_b32_e32 v165, 0
	v_mbcnt_lo_u32_b32 v131, -1, 0
	s_addc_u32 s11, s19, 0
	v_mbcnt_hi_u32_b32 v131, -1, v131
	s_add_u32 s8, s18, 0x108000
	s_addc_u32 s9, s19, 0
	s_add_u32 s12, s18, 0x106000
	s_addc_u32 s13, s19, 0
	s_mov_b64 s[20:21], 0x36c00000
	v_and_b32_e32 v235, 31, v0
	v_lshrrev_b32_e32 v192, 3, v0
	v_lshlrev_b32_e32 v130, 9, v130
	v_mov_b32_e32 v153, v165
	v_mov_b32_e32 v157, v165
	v_mov_b32_e32 v161, v165
	v_mov_b32_e32 v173, v165
	v_mov_b32_e32 v179, v165
	v_mov_b32_e32 v185, v165
	v_lshl_or_b32 v130, s96, 11, v130
	v_cmp_eq_u32_e64 s[4:5], 0, v162
	v_mov_b32_e32 v238, 0x358637bd
	s_mov_b32 s39, 0x800000
	s_mov_b32 s42, 0x42fe0000
	s_mov_b32 s43, 0xc0c0400
	s_mov_b32 s44, 0x5040100
	v_mov_b32_e32 v240, 1
	v_mov_b32_e32 v241, 0xff800000
	s_mov_b32 s45, s97
	s_waitcnt vmcnt(34)
	v_cvt_pk_bf16_f32 v4, v8, v9
	v_lshlrev_b32_e32 v50, 16, v4
	s_waitcnt vmcnt(32)
	v_cvt_pk_bf16_f32 v5, v10, v11
	v_lshlrev_b32_e32 v52, 16, v5
	v_and_b32_e32 v53, 0xffff0000, v5
	s_waitcnt vmcnt(29)
	v_cvt_pk_bf16_f32 v2, v14, v15
	v_lshlrev_b32_e32 v46, 16, v2
	s_waitcnt vmcnt(27)
	v_cvt_pk_bf16_f32 v3, v16, v17
	v_and_b32_e32 v47, 0xffff0000, v2
	v_lshlrev_b32_e32 v48, 16, v3
	v_and_b32_e32 v49, 0xffff0000, v3
	s_waitcnt vmcnt(23)
	v_cvt_pk_bf16_f32 v6, v12, v13
	v_lshlrev_b32_e32 v54, 16, v6
	v_and_b32_e32 v55, 0xffff0000, v6
	v_pk_add_f32 v[14:15], v[14:15], v[46:47] neg_lo:[0,1] neg_hi:[0,1]
	v_pk_add_f32 v[46:47], v[10:11], v[52:53] neg_lo:[0,1] neg_hi:[0,1]
	v_pk_add_f32 v[16:17], v[16:17], v[48:49] neg_lo:[0,1] neg_hi:[0,1]
	v_pk_add_f32 v[48:49], v[12:13], v[54:55] neg_lo:[0,1] neg_hi:[0,1]
	v_cvt_pk_bf16_f32 v13, v46, v47
	global_load_dword v46, v[38:39], off offset:320
	global_load_dword v47, v[38:39], off offset:448
	v_and_b32_e32 v51, 0xffff0000, v4
	v_pk_add_f32 v[8:9], v[8:9], v[50:51] neg_lo:[0,1] neg_hi:[0,1]
	v_cvt_pk_bf16_f32 v10, v14, v15
	v_cvt_pk_bf16_f32 v14, v48, v49
	global_load_dword v48, v[38:39], off offset:576
	global_load_dword v49, v[38:39], off offset:704
	global_load_dword v50, v[38:39], off offset:832
	global_load_dword v51, v[38:39], off offset:960
	global_load_dword v52, v[38:39], off offset:512
	global_load_dword v55, v[38:39], off offset:384
	global_load_dword v54, v[38:39], off offset:256
	global_load_dword v45, v[38:39], off offset:128
	v_cvt_pk_bf16_f32 v7, v20, v21
	v_lshlrev_b32_e32 v56, 16, v7
	v_and_b32_e32 v57, 0xffff0000, v7
	v_pk_add_f32 v[20:21], v[20:21], v[56:57] neg_lo:[0,1] neg_hi:[0,1]
	v_add_co_u32_e32 v56, vcc, s3, v84
	s_mov_b32 s3, 0x143000
	s_nop 0
	v_addc_co_u32_e32 v57, vcc, 0, v85, vcc
	global_load_dword v60, v[56:57], off
	global_load_dword v59, v[38:39], off offset:896
	global_load_dword v58, v[38:39], off offset:768
	global_load_dword v53, v[38:39], off offset:640
	global_load_dword v62, v[56:57], off offset:64
	global_load_dword v63, v[56:57], off offset:192
	global_load_dword v64, v[56:57], off offset:320
	global_load_dword v65, v[56:57], off offset:448
	global_load_dword v66, v[56:57], off offset:576
	global_load_dword v67, v[56:57], off offset:704
	global_load_dword v68, v[56:57], off offset:832
	global_load_dword v69, v[56:57], off offset:960
	global_load_dword v70, v[56:57], off offset:512
	global_load_dword v73, v[56:57], off offset:384
	global_load_dword v72, v[56:57], off offset:256
	global_load_dword v61, v[56:57], off offset:128
	v_add_co_u32_e32 v74, vcc, s3, v84
	v_cvt_pk_bf16_f32 v12, v8, v9
	s_nop 0
	v_addc_co_u32_e32 v75, vcc, 0, v85, vcc
	global_load_dword v76, v[74:75], off
	global_load_dword v79, v[56:57], off offset:896
	global_load_dword v78, v[56:57], off offset:768
	global_load_dword v71, v[56:57], off offset:640
	global_load_dword v80, v[74:75], off offset:64
	global_load_dword v81, v[74:75], off offset:192
	global_load_dword v82, v[74:75], off offset:320
	global_load_dword v83, v[74:75], off offset:448
	global_load_dword v86, v[74:75], off offset:576
	global_load_dword v87, v[74:75], off offset:704
	global_load_dword v88, v[74:75], off offset:832
	global_load_dword v89, v[74:75], off offset:960
	s_waitcnt vmcnt(57)
; DI unsigned pk2(float lo, float hi) { f32x2 v = {lo, hi}; bf16x2_t b = __builtin_convertvector(v, bf16x2_t); return __builtin_bit_cast(unsigned, b); }
; DI float bflo(unsigned w) { return __uint_as_float(w << 16); }
; DI float bfhi(unsigned w) { return __uint_as_float(w & 0xffff0000u); }
; __global__ void __launch_bounds__(NWAVES * 64, 2) fwd_kernel(Args a_unused) {
;     ...
;         bf16x8 bh[8][2], bl[8][2];
; #pragma unroll
;         for (int sK = 0; sK < 8; ++sK)
; #pragma unroll
;             for (int eh = 0; eh < 2; ++eh) { u32x4 ph, pl;
; #pragma unroll
;                 for (int i2 = 0; i2 < 4; ++i2) { const float w0 = wrp[(256 * wave + 32 * sK + 8 * kk + 2 * i2) * 32 + 16 * eh + r16], w1 = wrp[(256 * wave + 32 * sK + 8 * kk + 2 * i2 + 1) * 32 + 16 * eh + r16];
;                     const unsigned h = pk2(w0, w1); ph[i2] = h; pl[i2] = pk2(w0 - bflo(h), w1 - bfhi(h)); }
;                 bh[sK][eh] = __builtin_bit_cast(bf16x8, ph); bl[sK][eh] = __builtin_bit_cast(bf16x8, pl); }
	v_cvt_pk_bf16_f32 v8, v18, v19
	v_cvt_pk_bf16_f32 v11, v16, v17
	v_lshlrev_b32_e32 v16, 16, v8
	v_and_b32_e32 v17, 0xffff0000, v8
	v_cvt_pk_bf16_f32 v9, v30, v31
	v_pk_add_f32 v[16:17], v[18:19], v[16:17] neg_lo:[0,1] neg_hi:[0,1]
	v_lshlrev_b32_e32 v18, 16, v9
	v_and_b32_e32 v19, 0xffff0000, v9
	v_pk_add_f32 v[18:19], v[30:31], v[18:19] neg_lo:[0,1] neg_hi:[0,1]
	v_cvt_pk_bf16_f32 v16, v16, v17
	v_cvt_pk_bf16_f32 v17, v18, v19
	s_waitcnt vmcnt(55)
	v_cvt_pk_bf16_f32 v18, v22, v23
	v_cvt_pk_bf16_f32 v15, v20, v21
	v_lshlrev_b32_e32 v20, 16, v18
	v_and_b32_e32 v21, 0xffff0000, v18
	v_pk_add_f32 v[20:21], v[22:23], v[20:21] neg_lo:[0,1] neg_hi:[0,1]
	s_waitcnt vmcnt(53)
	v_cvt_pk_bf16_f32 v19, v26, v27
	v_cvt_pk_bf16_f32 v22, v20, v21
	v_lshlrev_b32_e32 v20, 16, v19
	v_and_b32_e32 v21, 0xffff0000, v19
	v_pk_add_f32 v[20:21], v[26:27], v[20:21] neg_lo:[0,1] neg_hi:[0,1]
	global_load_dword v90, v[74:75], off offset:512
	global_load_dword v93, v[74:75], off offset:384
	global_load_dword v92, v[74:75], off offset:256
	global_load_dword v77, v[74:75], off offset:128
	v_cvt_pk_bf16_f32 v23, v20, v21
	s_waitcnt vmcnt(55)
	v_cvt_pk_bf16_f32 v20, v24, v25
	v_lshlrev_b32_e32 v26, 16, v20
	v_and_b32_e32 v27, 0xffff0000, v20
	s_waitcnt vmcnt(53)
	v_cvt_pk_bf16_f32 v21, v36, v37
	v_pk_add_f32 v[24:25], v[24:25], v[26:27] neg_lo:[0,1] neg_hi:[0,1]
	v_lshlrev_b32_e32 v26, 16, v21
	v_and_b32_e32 v27, 0xffff0000, v21
	v_pk_add_f32 v[26:27], v[36:37], v[26:27] neg_lo:[0,1] neg_hi:[0,1]
	v_cvt_pk_bf16_f32 v24, v24, v25
	v_cvt_pk_bf16_f32 v25, v26, v27
	s_waitcnt vmcnt(49)
	v_cvt_pk_bf16_f32 v26, v28, v29
	v_lshlrev_b32_e32 v30, 16, v26
	v_and_b32_e32 v31, 0xffff0000, v26
	v_pk_add_f32 v[28:29], v[28:29], v[30:31] neg_lo:[0,1] neg_hi:[0,1]
	v_cvt_pk_bf16_f32 v27, v34, v35
	v_cvt_pk_bf16_f32 v30, v28, v29
	v_lshlrev_b32_e32 v28, 16, v27
	v_and_b32_e32 v29, 0xffff0000, v27
	v_pk_add_f32 v[28:29], v[34:35], v[28:29] neg_lo:[0,1] neg_hi:[0,1]
	s_mov_b32 s3, 0x142000
	v_cvt_pk_bf16_f32 v31, v28, v29
	s_waitcnt vmcnt(45)
	v_cvt_pk_bf16_f32 v28, v32, v33
	v_lshlrev_b32_e32 v34, 16, v28
	v_and_b32_e32 v35, 0xffff0000, v28
	v_cvt_pk_bf16_f32 v29, v42, v43
	v_pk_add_f32 v[32:33], v[32:33], v[34:35] neg_lo:[0,1] neg_hi:[0,1]
	v_lshlrev_b32_e32 v34, 16, v29
	v_and_b32_e32 v35, 0xffff0000, v29
	v_pk_add_f32 v[34:35], v[42:43], v[34:35] neg_lo:[0,1] neg_hi:[0,1]
	v_cvt_pk_bf16_f32 v32, v32, v33
	v_cvt_pk_bf16_f32 v33, v34, v35
	s_waitcnt vmcnt(43)
	v_cvt_pk_bf16_f32 v34, v40, v41
	v_lshlrev_b32_e32 v36, 16, v34
	v_and_b32_e32 v37, 0xffff0000, v34
	v_pk_add_f32 v[36:37], v[40:41], v[36:37] neg_lo:[0,1] neg_hi:[0,1]
	s_waitcnt vmcnt(40)
	v_cvt_pk_bf16_f32 v35, v46, v47
	v_cvt_pk_bf16_f32 v38, v36, v37
	v_lshlrev_b32_e32 v36, 16, v35
	v_and_b32_e32 v37, 0xffff0000, v35
	v_pk_add_f32 v[36:37], v[46:47], v[36:37] neg_lo:[0,1] neg_hi:[0,1]
	v_add_co_u32_e32 v94, vcc, s3, v84
	v_cvt_pk_bf16_f32 v39, v36, v37
	s_waitcnt vmcnt(38)
	v_cvt_pk_bf16_f32 v36, v48, v49
	s_waitcnt vmcnt(36)
	v_cvt_pk_bf16_f32 v37, v50, v51
	v_lshlrev_b32_e32 v40, 16, v36
	v_and_b32_e32 v41, 0xffff0000, v36
	v_lshlrev_b32_e32 v42, 16, v37
	v_and_b32_e32 v43, 0xffff0000, v37
	v_pk_add_f32 v[40:41], v[48:49], v[40:41] neg_lo:[0,1] neg_hi:[0,1]
	v_pk_add_f32 v[42:43], v[50:51], v[42:43] neg_lo:[0,1] neg_hi:[0,1]
	v_cvt_pk_bf16_f32 v40, v40, v41
	v_cvt_pk_bf16_f32 v41, v42, v43
	s_waitcnt vmcnt(32)
	v_cvt_pk_bf16_f32 v42, v44, v45
	v_lshlrev_b32_e32 v46, 16, v42
	v_and_b32_e32 v47, 0xffff0000, v42
	v_pk_add_f32 v[44:45], v[44:45], v[46:47] neg_lo:[0,1] neg_hi:[0,1]
	v_cvt_pk_bf16_f32 v43, v54, v55
	v_cvt_pk_bf16_f32 v46, v44, v45
	v_lshlrev_b32_e32 v44, 16, v43
	v_and_b32_e32 v45, 0xffff0000, v43
	v_pk_add_f32 v[44:45], v[54:55], v[44:45] neg_lo:[0,1] neg_hi:[0,1]
	v_addc_co_u32_e32 v95, vcc, 0, v85, vcc
	v_cvt_pk_bf16_f32 v47, v44, v45
	s_waitcnt vmcnt(28)
	v_cvt_pk_bf16_f32 v44, v52, v53
	v_cvt_pk_bf16_f32 v45, v58, v59
	v_lshlrev_b32_e32 v48, 16, v44
	v_and_b32_e32 v49, 0xffff0000, v44
	v_lshlrev_b32_e32 v50, 16, v45
	v_and_b32_e32 v51, 0xffff0000, v45
	v_pk_add_f32 v[48:49], v[52:53], v[48:49] neg_lo:[0,1] neg_hi:[0,1]
	v_pk_add_f32 v[50:51], v[58:59], v[50:51] neg_lo:[0,1] neg_hi:[0,1]
	v_cvt_pk_bf16_f32 v48, v48, v49
	v_cvt_pk_bf16_f32 v49, v50, v51
	s_waitcnt vmcnt(26)
	v_cvt_pk_bf16_f32 v50, v62, v63
	v_lshlrev_b32_e32 v52, 16, v50
	v_and_b32_e32 v53, 0xffff0000, v50
	v_pk_add_f32 v[52:53], v[62:63], v[52:53] neg_lo:[0,1] neg_hi:[0,1]
	s_waitcnt vmcnt(24)
	v_cvt_pk_bf16_f32 v51, v64, v65
	v_cvt_pk_bf16_f32 v54, v52, v53
	v_lshlrev_b32_e32 v52, 16, v51
	v_and_b32_e32 v53, 0xffff0000, v51
	v_pk_add_f32 v[52:53], v[64:65], v[52:53] neg_lo:[0,1] neg_hi:[0,1]
	global_load_dword v98, v[94:95], off
	global_load_dword v101, v[74:75], off offset:896
	global_load_dword v100, v[74:75], off offset:768
	global_load_dword v91, v[74:75], off offset:640
	v_cvt_pk_bf16_f32 v55, v52, v53
	s_waitcnt vmcnt(26)
	v_cvt_pk_bf16_f32 v52, v66, v67
	s_waitcnt vmcnt(24)
	v_cvt_pk_bf16_f32 v53, v68, v69
	v_lshlrev_b32_e32 v56, 16, v52
	v_and_b32_e32 v57, 0xffff0000, v52
	v_lshlrev_b32_e32 v58, 16, v53
	v_and_b32_e32 v59, 0xffff0000, v53
	v_pk_add_f32 v[56:57], v[66:67], v[56:57] neg_lo:[0,1] neg_hi:[0,1]
	v_pk_add_f32 v[58:59], v[68:69], v[58:59] neg_lo:[0,1] neg_hi:[0,1]
	v_cvt_pk_bf16_f32 v56, v56, v57
	v_cvt_pk_bf16_f32 v57, v58, v59
	s_waitcnt vmcnt(20)
	v_cvt_pk_bf16_f32 v58, v60, v61
	v_lshlrev_b32_e32 v62, 16, v58
	v_and_b32_e32 v63, 0xffff0000, v58
	v_pk_add_f32 v[60:61], v[60:61], v[62:63] neg_lo:[0,1] neg_hi:[0,1]
	v_cvt_pk_bf16_f32 v59, v72, v73
	v_cvt_pk_bf16_f32 v62, v60, v61
	v_lshlrev_b32_e32 v60, 16, v59
	v_and_b32_e32 v61, 0xffff0000, v59
	v_pk_add_f32 v[60:61], v[72:73], v[60:61] neg_lo:[0,1] neg_hi:[0,1]
	global_load_dword v102, v[94:95], off offset:64
	global_load_dword v103, v[94:95], off offset:192
	v_cvt_pk_bf16_f32 v63, v60, v61
	s_waitcnt vmcnt(18)
; DI unsigned pk2(float lo, float hi) { f32x2 v = {lo, hi}; bf16x2_t b = __builtin_convertvector(v, bf16x2_t); return __builtin_bit_cast(unsigned, b); }
; DI float bflo(unsigned w) { return __uint_as_float(w << 16); }
; DI float bfhi(unsigned w) { return __uint_as_float(w & 0xffff0000u); }
; __global__ void __launch_bounds__(NWAVES * 64, 2) fwd_kernel(Args a_unused) {
;     ...
;         bf16x8 bh[8][2], bl[8][2];
; #pragma unroll
;         for (int sK = 0; sK < 8; ++sK)
; #pragma unroll
;             for (int eh = 0; eh < 2; ++eh) { u32x4 ph, pl;
; #pragma unroll
;                 for (int i2 = 0; i2 < 4; ++i2) { const float w0 = wrp[(256 * wave + 32 * sK + 8 * kk + 2 * i2) * 32 + 16 * eh + r16], w1 = wrp[(256 * wave + 32 * sK + 8 * kk + 2 * i2 + 1) * 32 + 16 * eh + r16];
;                     const unsigned h = pk2(w0, w1); ph[i2] = h; pl[i2] = pk2(w0 - bflo(h), w1 - bfhi(h)); }
;                 bh[sK][eh] = __builtin_bit_cast(bf16x8, ph); bl[sK][eh] = __builtin_bit_cast(bf16x8, pl); }
	v_cvt_pk_bf16_f32 v60, v70, v71
	v_cvt_pk_bf16_f32 v61, v78, v79
	v_lshlrev_b32_e32 v64, 16, v60
	v_and_b32_e32 v65, 0xffff0000, v60
	v_lshlrev_b32_e32 v66, 16, v61
	v_and_b32_e32 v67, 0xffff0000, v61
	global_load_dword v104, v[94:95], off offset:320
	global_load_dword v105, v[94:95], off offset:448
	v_pk_add_f32 v[64:65], v[70:71], v[64:65] neg_lo:[0,1] neg_hi:[0,1]
	v_pk_add_f32 v[66:67], v[78:79], v[66:67] neg_lo:[0,1] neg_hi:[0,1]
	v_cvt_pk_bf16_f32 v64, v64, v65
	v_cvt_pk_bf16_f32 v65, v66, v67
	s_waitcnt vmcnt(18)
	v_cvt_pk_bf16_f32 v66, v80, v81
	v_lshlrev_b32_e32 v68, 16, v66
	v_and_b32_e32 v69, 0xffff0000, v66
	global_load_dword v106, v[94:95], off offset:576
	global_load_dword v107, v[94:95], off offset:704
	global_load_dword v108, v[94:95], off offset:832
	global_load_dword v109, v[94:95], off offset:960
	v_pk_add_f32 v[68:69], v[80:81], v[68:69] neg_lo:[0,1] neg_hi:[0,1]
	s_waitcnt vmcnt(20)
	v_cvt_pk_bf16_f32 v67, v82, v83
	v_cvt_pk_bf16_f32 v70, v68, v69
	v_lshlrev_b32_e32 v68, 16, v67
	v_and_b32_e32 v69, 0xffff0000, v67
	v_pk_add_f32 v[68:69], v[82:83], v[68:69] neg_lo:[0,1] neg_hi:[0,1]
	global_load_dword v110, v[94:95], off offset:512
	global_load_dword v113, v[94:95], off offset:384
	global_load_dword v112, v[94:95], off offset:256
	global_load_dword v99, v[94:95], off offset:128
	v_cvt_pk_bf16_f32 v71, v68, v69
	s_waitcnt vmcnt(20)
	v_cvt_pk_bf16_f32 v69, v88, v89
	v_lshlrev_b32_e32 v74, 16, v69
	v_and_b32_e32 v75, 0xffff0000, v69
	s_mov_b32 s3, 0x141000
	v_pk_add_f32 v[74:75], v[88:89], v[74:75] neg_lo:[0,1] neg_hi:[0,1]
	v_add_co_u32_e32 v88, vcc, s3, v84
	s_mov_b32 s3, 0x140000
	s_nop 0
	v_addc_co_u32_e32 v89, vcc, 0, v85, vcc
	global_load_dword v114, v[88:89], off
	global_load_dword v117, v[94:95], off offset:896
	global_load_dword v116, v[94:95], off offset:768
	global_load_dword v111, v[94:95], off offset:640
	global_load_dword v118, v[88:89], off offset:64
	global_load_dword v119, v[88:89], off offset:192
	global_load_dword v120, v[88:89], off offset:320
	global_load_dword v121, v[88:89], off offset:448
	global_load_dword v124, v[88:89], off offset:576
	global_load_dword v125, v[88:89], off offset:704
	global_load_dword v126, v[88:89], off offset:832
	global_load_dword v127, v[88:89], off offset:960
	global_load_dword v128, v[88:89], off offset:512
	global_load_dword v133, v[88:89], off offset:384
	global_load_dword v132, v[88:89], off offset:256
	global_load_dword v115, v[88:89], off offset:128
	v_add_co_u32_e32 v84, vcc, s3, v84
	v_cvt_pk_bf16_f32 v68, v86, v87
	s_nop 0
	v_addc_co_u32_e32 v85, vcc, 0, v85, vcc
	global_load_dword v134, v[84:85], off
	global_load_dword v137, v[88:89], off offset:896
	global_load_dword v136, v[88:89], off offset:768
	global_load_dword v129, v[88:89], off offset:640
	global_load_dword v138, v[96:97], off offset:64
	global_load_dword v139, v[96:97], off offset:192
	global_load_dword v140, v[96:97], off offset:320
	global_load_dword v141, v[96:97], off offset:448
	global_load_dword v142, v[96:97], off offset:576
	global_load_dword v143, v[96:97], off offset:704
	global_load_dword v122, v[96:97], off offset:832
	global_load_dword v144, v[96:97], off offset:512
	global_load_dword v147, v[96:97], off offset:384
	global_load_dword v146, v[96:97], off offset:256
	global_load_dword v135, v[96:97], off offset:128
	global_load_dword v149, v[96:97], off offset:896
	global_load_dword v148, v[96:97], off offset:768
	global_load_dword v145, v[96:97], off offset:640
	v_lshlrev_b32_e32 v72, 16, v68
	v_and_b32_e32 v73, 0xffff0000, v68
	v_pk_add_f32 v[72:73], v[86:87], v[72:73] neg_lo:[0,1] neg_hi:[0,1]
	s_lshl_b32 s3, s96, 3
	v_cvt_pk_bf16_f32 v72, v72, v73
	v_cvt_pk_bf16_f32 v73, v74, v75
	s_waitcnt vmcnt(50)
	v_cvt_pk_bf16_f32 v74, v76, v77
	v_lshlrev_b32_e32 v78, 16, v74
	v_and_b32_e32 v79, 0xffff0000, v74
	v_pk_add_f32 v[76:77], v[76:77], v[78:79] neg_lo:[0,1] neg_hi:[0,1]
	v_cvt_pk_bf16_f32 v75, v92, v93
	v_cvt_pk_bf16_f32 v78, v76, v77
	v_lshlrev_b32_e32 v76, 16, v75
	v_and_b32_e32 v77, 0xffff0000, v75
	v_pk_add_f32 v[76:77], v[92:93], v[76:77] neg_lo:[0,1] neg_hi:[0,1]
	s_add_i32 s31, s3, 0
	v_cvt_pk_bf16_f32 v79, v76, v77
	s_waitcnt vmcnt(46)
	v_cvt_pk_bf16_f32 v76, v90, v91
	v_cvt_pk_bf16_f32 v77, v100, v101
	v_lshlrev_b32_e32 v80, 16, v76
	v_and_b32_e32 v81, 0xffff0000, v76
	v_lshlrev_b32_e32 v82, 16, v77
	v_and_b32_e32 v83, 0xffff0000, v77
	v_pk_add_f32 v[80:81], v[90:91], v[80:81] neg_lo:[0,1] neg_hi:[0,1]
	v_pk_add_f32 v[82:83], v[100:101], v[82:83] neg_lo:[0,1] neg_hi:[0,1]
	v_cvt_pk_bf16_f32 v80, v80, v81
	v_cvt_pk_bf16_f32 v81, v82, v83
	s_waitcnt vmcnt(44)
	v_cvt_pk_bf16_f32 v82, v102, v103
	v_lshlrev_b32_e32 v86, 16, v82
	v_and_b32_e32 v87, 0xffff0000, v82
	v_pk_add_f32 v[86:87], v[102:103], v[86:87] neg_lo:[0,1] neg_hi:[0,1]
	s_add_u32 s34, s18, 0xf80000
	v_cvt_pk_bf16_f32 v86, v86, v87
	s_addc_u32 s35, s19, 0
	s_waitcnt vmcnt(42)
	v_cvt_pk_bf16_f32 v83, v104, v105
	v_lshlrev_b32_e32 v84, 16, v83
	v_and_b32_e32 v85, 0xffff0000, v83
	v_pk_add_f32 v[84:85], v[104:105], v[84:85] neg_lo:[0,1] neg_hi:[0,1]
	s_lshl_b32 s3, s96, 9
	v_cvt_pk_bf16_f32 v87, v84, v85
	s_load_dwordx2 s[6:7], s[16:17], 0x28
	s_waitcnt vmcnt(40)
	v_cvt_pk_bf16_f32 v84, v106, v107
	s_waitcnt vmcnt(38)
	v_cvt_pk_bf16_f32 v85, v108, v109
	v_lshlrev_b32_e32 v88, 16, v84
	v_and_b32_e32 v89, 0xffff0000, v84
	v_lshlrev_b32_e32 v90, 16, v85
	v_and_b32_e32 v91, 0xffff0000, v85
	v_pk_add_f32 v[88:89], v[106:107], v[88:89] neg_lo:[0,1] neg_hi:[0,1]
	v_pk_add_f32 v[90:91], v[108:109], v[90:91] neg_lo:[0,1] neg_hi:[0,1]
	v_cvt_pk_bf16_f32 v88, v88, v89
	v_cvt_pk_bf16_f32 v89, v90, v91
	s_waitcnt vmcnt(34)
; DI unsigned pk2(float lo, float hi) { f32x2 v = {lo, hi}; bf16x2_t b = __builtin_convertvector(v, bf16x2_t); return __builtin_bit_cast(unsigned, b); }
; DI float bflo(unsigned w) { return __uint_as_float(w << 16); }
; DI float bfhi(unsigned w) { return __uint_as_float(w & 0xffff0000u); }
; __global__ void __launch_bounds__(NWAVES * 64, 2) fwd_kernel(Args a_unused) {
;     ...
;         bf16x8 bh[8][2], bl[8][2];
; #pragma unroll
;         for (int sK = 0; sK < 8; ++sK)
; #pragma unroll
;             for (int eh = 0; eh < 2; ++eh) { u32x4 ph, pl;
; #pragma unroll
;                 for (int i2 = 0; i2 < 4; ++i2) { const float w0 = wrp[(256 * wave + 32 * sK + 8 * kk + 2 * i2) * 32 + 16 * eh + r16], w1 = wrp[(256 * wave + 32 * sK + 8 * kk + 2 * i2 + 1) * 32 + 16 * eh + r16];
;                     const unsigned h = pk2(w0, w1); ph[i2] = h; pl[i2] = pk2(w0 - bflo(h), w1 - bfhi(h)); }
;                 bh[sK][eh] = __builtin_bit_cast(bf16x8, ph); bl[sK][eh] = __builtin_bit_cast(bf16x8, pl); }
	v_cvt_pk_bf16_f32 v90, v98, v99
	v_lshlrev_b32_e32 v92, 16, v90
	v_and_b32_e32 v93, 0xffff0000, v90
	v_pk_add_f32 v[92:93], v[98:99], v[92:93] neg_lo:[0,1] neg_hi:[0,1]
	v_cvt_pk_bf16_f32 v91, v112, v113
	v_cvt_pk_bf16_f32 v94, v92, v93
	v_lshlrev_b32_e32 v92, 16, v91
	v_and_b32_e32 v93, 0xffff0000, v91
	v_pk_add_f32 v[92:93], v[112:113], v[92:93] neg_lo:[0,1] neg_hi:[0,1]
	s_nop 0
	v_cvt_pk_bf16_f32 v95, v92, v93
	s_waitcnt vmcnt(30)
	v_cvt_pk_bf16_f32 v92, v110, v111
	v_cvt_pk_bf16_f32 v93, v116, v117
	v_lshlrev_b32_e32 v96, 16, v92
	v_and_b32_e32 v97, 0xffff0000, v92
	v_lshlrev_b32_e32 v98, 16, v93
	v_and_b32_e32 v99, 0xffff0000, v93
	v_pk_add_f32 v[96:97], v[110:111], v[96:97] neg_lo:[0,1] neg_hi:[0,1]
	v_pk_add_f32 v[98:99], v[116:117], v[98:99] neg_lo:[0,1] neg_hi:[0,1]
	v_cvt_pk_bf16_f32 v96, v96, v97
	v_cvt_pk_bf16_f32 v97, v98, v99
	s_waitcnt vmcnt(28)
	v_cvt_pk_bf16_f32 v98, v118, v119
	v_lshlrev_b32_e32 v100, 16, v98
	v_and_b32_e32 v101, 0xffff0000, v98
	v_pk_add_f32 v[100:101], v[118:119], v[100:101] neg_lo:[0,1] neg_hi:[0,1]
	s_waitcnt vmcnt(26)
	v_cvt_pk_bf16_f32 v99, v120, v121
	v_cvt_pk_bf16_f32 v102, v100, v101
	v_lshlrev_b32_e32 v100, 16, v99
	v_and_b32_e32 v101, 0xffff0000, v99
	v_pk_add_f32 v[100:101], v[120:121], v[100:101] neg_lo:[0,1] neg_hi:[0,1]
	s_nop 0
	v_cvt_pk_bf16_f32 v103, v100, v101
	s_waitcnt vmcnt(24)
	v_cvt_pk_bf16_f32 v100, v124, v125
	s_waitcnt vmcnt(22)
	v_cvt_pk_bf16_f32 v101, v126, v127
	v_lshlrev_b32_e32 v104, 16, v100
	v_and_b32_e32 v105, 0xffff0000, v100
	v_lshlrev_b32_e32 v106, 16, v101
	v_and_b32_e32 v107, 0xffff0000, v101
	v_pk_add_f32 v[104:105], v[124:125], v[104:105] neg_lo:[0,1] neg_hi:[0,1]
	v_pk_add_f32 v[106:107], v[126:127], v[106:107] neg_lo:[0,1] neg_hi:[0,1]
	v_cvt_pk_bf16_f32 v104, v104, v105
	v_cvt_pk_bf16_f32 v105, v106, v107
	s_waitcnt vmcnt(18)
	v_cvt_pk_bf16_f32 v106, v114, v115
	v_lshlrev_b32_e32 v108, 16, v106
	v_and_b32_e32 v109, 0xffff0000, v106
	v_pk_add_f32 v[108:109], v[114:115], v[108:109] neg_lo:[0,1] neg_hi:[0,1]
	v_cvt_pk_bf16_f32 v107, v132, v133
	v_cvt_pk_bf16_f32 v110, v108, v109
	v_lshlrev_b32_e32 v108, 16, v107
	v_and_b32_e32 v109, 0xffff0000, v107
	v_pk_add_f32 v[108:109], v[132:133], v[108:109] neg_lo:[0,1] neg_hi:[0,1]
	s_nop 0
	v_cvt_pk_bf16_f32 v111, v108, v109
	s_waitcnt vmcnt(14)
	v_cvt_pk_bf16_f32 v108, v128, v129
	v_cvt_pk_bf16_f32 v109, v136, v137
	v_lshlrev_b32_e32 v112, 16, v108
	v_and_b32_e32 v113, 0xffff0000, v108
	v_lshlrev_b32_e32 v114, 16, v109
	v_and_b32_e32 v115, 0xffff0000, v109
	v_pk_add_f32 v[112:113], v[128:129], v[112:113] neg_lo:[0,1] neg_hi:[0,1]
	v_pk_add_f32 v[114:115], v[136:137], v[114:115] neg_lo:[0,1] neg_hi:[0,1]
	v_cvt_pk_bf16_f32 v112, v112, v113
	v_cvt_pk_bf16_f32 v113, v114, v115
	s_waitcnt vmcnt(12)
	v_cvt_pk_bf16_f32 v114, v138, v139
	v_lshlrev_b32_e32 v116, 16, v114
	v_and_b32_e32 v117, 0xffff0000, v114
	v_pk_add_f32 v[116:117], v[138:139], v[116:117] neg_lo:[0,1] neg_hi:[0,1]
	s_waitcnt vmcnt(10)
	v_cvt_pk_bf16_f32 v115, v140, v141
	v_cvt_pk_bf16_f32 v118, v116, v117
	v_lshlrev_b32_e32 v116, 16, v115
	v_and_b32_e32 v117, 0xffff0000, v115
	v_pk_add_f32 v[116:117], v[140:141], v[116:117] neg_lo:[0,1] neg_hi:[0,1]
	s_nop 0
	v_cvt_pk_bf16_f32 v119, v116, v117
	s_waitcnt vmcnt(8)
	v_cvt_pk_bf16_f32 v116, v142, v143
	s_waitcnt vmcnt(7)
	v_cvt_pk_bf16_f32 v117, v122, v123
	v_lshlrev_b32_e32 v120, 16, v116
	v_and_b32_e32 v121, 0xffff0000, v116
	v_lshlrev_b32_e32 v124, 16, v117
	v_and_b32_e32 v125, 0xffff0000, v117
	v_pk_add_f32 v[120:121], v[142:143], v[120:121] neg_lo:[0,1] neg_hi:[0,1]
	v_pk_add_f32 v[122:123], v[122:123], v[124:125] neg_lo:[0,1] neg_hi:[0,1]
	v_cvt_pk_bf16_f32 v120, v120, v121
	v_cvt_pk_bf16_f32 v121, v122, v123
	s_waitcnt vmcnt(3)
	v_cvt_pk_bf16_f32 v122, v134, v135
	v_lshlrev_b32_e32 v124, 16, v122
	v_and_b32_e32 v125, 0xffff0000, v122
	v_pk_add_f32 v[124:125], v[134:135], v[124:125] neg_lo:[0,1] neg_hi:[0,1]
	v_cvt_pk_bf16_f32 v123, v146, v147
	v_cvt_pk_bf16_f32 v126, v124, v125
	v_lshlrev_b32_e32 v124, 16, v123
	v_and_b32_e32 v125, 0xffff0000, v123
	v_pk_add_f32 v[124:125], v[146:147], v[124:125] neg_lo:[0,1] neg_hi:[0,1]
	s_nop 0
	v_cvt_pk_bf16_f32 v127, v124, v125
	s_waitcnt vmcnt(0)
; DI float bflo(unsigned w) { return __uint_as_float(w << 16); }
; DI float bfhi(unsigned w) { return __uint_as_float(w & 0xffff0000u); }
; __global__ void __launch_bounds__(NWAVES * 64, 2) fwd_kernel(Args a_unused) {
;     ...
;         for (int tl = vcu; tl < NTOK / 16; tl += G) {
;             const int row0 = tl * 16;
; #pragma unroll
;             for (int q = 0; q < 2; ++q) { const int m = row0 + 2 * wave + q; const unsigned short* xr = X1 + (size_t)m * D + 4 * lane; f32x4 v[8]; float ss = 0.f;
; #pragma unroll
;                 for (int j = 0; j < 8; ++j) { const u32x2 w2 = *(const u32x2*)(xr + 256 * j); v[j] = (f32x4){bflo(w2[0]), bfhi(w2[0]), bflo(w2[1]), bfhi(w2[1])}; ss += v[j][0] * v[j][0] + v[j][1] * v[j][1] + v[j][2] * v[j][2] + v[j][3] * v[j][3]; }
;                 const float rstd = rsqrtf(wave_sum(ss) * (1.0f / D) + EPS);
;                 if (lane == 0) rsd[2 * wave + q] = rstd;
;                 float am = 0.f;
; #pragma unroll
;                 for (int j = 0; j < 8; ++j) { const int k = 4 * lane + 256 * j; const f32x4 g = *(const f32x4*)(A->norm_ffn_g + k), s1 = *(const f32x4*)(modl + 4 * 2048 + k), s0 = *(const f32x4*)(modl + 3 * 2048 + k);
;                     v[j] = v[j] * rstd * (g * (1.0f + s1)) + s0; am = fmaxf(am, fmaxf(fmaxf(fabsf(v[j][0]), fabsf(v[j][1])), fmaxf(fabsf(v[j][2]), fabsf(v[j][3])))); }
; #pragma unroll
;                 for (int o = 1; o < 64; o <<= 1) am = fmaxf(am, __shfl_xor(am, o));
;                 if (am == 0.f) am = 1.f;
;                 const float qi = 127.0f / am;
;                 if (lane == 0) ((float*)(ws + WS_CS + CS_ROW))[m] = am * (1.0f / 127.0f);
;                 unsigned* hq = (unsigned*)((signed char*)(ws + WS_H) + (size_t)m * D + 4 * lane);
; #pragma unroll
;                 for (int j = 0; j < 8; ++j) hq[64 * j] = q8x4(v[j][0], v[j][1], v[j][2], v[j][3], qi); }
;             f32x4 acc0 = {0.f, 0.f, 0.f, 0.f}, acc1 = {0.f, 0.f, 0.f, 0.f};
;             const unsigned short* xa = X1 + (size_t)(row0 + r16) * D + 256 * wave + 8 * kk;
	v_cvt_pk_bf16_f32 v124, v144, v145
	v_cvt_pk_bf16_f32 v125, v148, v149
	v_lshlrev_b32_e32 v128, 16, v124
	v_and_b32_e32 v129, 0xffff0000, v124
	v_lshlrev_b32_e32 v132, 16, v125
	v_and_b32_e32 v133, 0xffff0000, v125
	v_pk_add_f32 v[128:129], v[144:145], v[128:129] neg_lo:[0,1] neg_hi:[0,1]
	v_pk_add_f32 v[132:133], v[148:149], v[132:133] neg_lo:[0,1] neg_hi:[0,1]
	v_cvt_pk_bf16_f32 v128, v128, v129
	v_cvt_pk_bf16_f32 v129, v132, v133
	v_lshlrev_b32_e32 v132, 3, v162
	v_mov_b32_e32 v133, v165
	v_lshl_add_u64 v[134:135], s[10:11], 0, v[132:133]
	v_and_b32_e32 v132, 64, v131
	v_add_u32_e32 v132, 64, v132
	v_xor_b32_e32 v133, 1, v131
	v_cmp_lt_i32_e32 vcc, v133, v132
	s_add_u32 s10, s10, s3
	s_addc_u32 s11, s11, 0
	v_cndmask_b32_e32 v133, v131, v133, vcc
	v_lshlrev_b32_e32 v163, 2, v133
	v_xor_b32_e32 v133, 2, v131
	v_cmp_lt_i32_e32 vcc, v133, v132
	s_nop 1
	v_cndmask_b32_e32 v133, v131, v133, vcc
	v_lshlrev_b32_e32 v167, 2, v133
	v_xor_b32_e32 v133, 4, v131
	v_cmp_lt_i32_e32 vcc, v133, v132
	s_nop 1
	v_cndmask_b32_e32 v133, v131, v133, vcc
	v_lshlrev_b32_e32 v207, 2, v133
	v_xor_b32_e32 v133, 8, v131
	v_cmp_lt_i32_e32 vcc, v133, v132
	s_nop 1
	v_cndmask_b32_e32 v133, v131, v133, vcc
	v_lshlrev_b32_e32 v232, 2, v133
	v_xor_b32_e32 v133, 16, v131
	v_cmp_lt_i32_e32 vcc, v133, v132
	s_nop 1
	v_cndmask_b32_e32 v133, v131, v133, vcc
	v_lshlrev_b32_e32 v233, 2, v133
	v_xor_b32_e32 v133, 32, v131
	v_cmp_lt_i32_e32 vcc, v133, v132
	s_nop 1
	v_cndmask_b32_e32 v131, v131, v133, vcc
	v_lshl_add_u64 v[132:133], s[18:19], 0, v[164:165]
	v_lshl_add_u64 v[136:137], v[132:133], 0, s[20:21]
	v_and_b32_e32 v132, 48, v162
	v_mov_b32_e32 v133, v165
	v_lshl_add_u64 v[138:139], s[10:11], 0, v[132:133]
	v_and_b32_e32 v132, 0x1e0, v0
	v_lshlrev_b32_e32 v133, 2, v132
	v_lshlrev_b32_e32 v132, 2, v235
	v_add3_u32 v236, 0, v133, v132
	v_and_b32_e32 v133, 60, v192
	v_add_u32_e32 v237, 0, v133
	v_mov_b32_e32 v133, v165
	s_add_u32 s20, s18, 0x200000
	v_lshl_add_u64 v[132:133], s[18:19], 0, v[132:133]
	s_mov_b64 s[10:11], 0x180000
	s_addc_u32 s21, s19, 0
	v_lshl_add_u64 v[140:141], v[132:133], 0, s[10:11]
	v_lshlrev_b32_e32 v132, 6, v235
	v_mov_b32_e32 v133, v165
	s_add_u32 s22, s18, 0x240000
	v_lshl_add_u64 v[132:133], s[48:49], 0, v[132:133]
	s_mov_b64 s[10:11], 0x8000
	s_addc_u32 s23, s19, 0
	v_lshl_add_u64 v[142:143], v[132:133], 0, s[10:11]
	s_add_u32 s24, s18, 0x280000
	v_lshlrev_b32_e32 v132, 4, v162
	v_mov_b32_e32 v133, v165
	v_lshlrev_b32_e32 v234, 2, v131
	v_lshl_add_u32 v131, v1, 2, 0
	s_addc_u32 s25, s19, 0
	s_waitcnt lgkmcnt(0)
	v_lshl_add_u64 v[144:145], s[6:7], 0, v[132:133]
	v_lshl_add_u64 v[146:147], s[8:9], 0, v[132:133]
	v_lshl_add_u64 v[148:149], s[12:13], 0, v[132:133]
	v_or_b32_e32 v152, 0x400, v132
	v_or_b32_e32 v156, 0x800, v132
	v_or_b32_e32 v160, 0xc00, v132
	v_or_b32_e32 v172, 0x1000, v132
	v_or_b32_e32 v178, 0x1400, v132
	v_or_b32_e32 v184, 0x1800, v132
	v_or_b32_e32 v132, 0x1c00, v132
	s_lshl_b32 s3, s97, 6
	v_lshl_add_u64 v[150:151], s[8:9], 0, v[152:153]
	v_lshl_add_u64 v[152:153], s[12:13], 0, v[152:153]
	v_lshl_add_u64 v[154:155], s[8:9], 0, v[156:157]
	v_lshl_add_u64 v[156:157], s[12:13], 0, v[156:157]
	v_lshl_add_u64 v[158:159], s[8:9], 0, v[160:161]
	v_lshl_add_u64 v[160:161], s[12:13], 0, v[160:161]
	v_lshl_add_u64 v[168:169], s[6:7], 0, v[172:173]
	v_lshl_add_u64 v[170:171], s[8:9], 0, v[172:173]
	v_lshl_add_u64 v[172:173], s[12:13], 0, v[172:173]
	v_lshl_add_u64 v[174:175], s[6:7], 0, v[178:179]
	v_lshl_add_u64 v[176:177], s[8:9], 0, v[178:179]
	v_lshl_add_u64 v[178:179], s[12:13], 0, v[178:179]
	v_lshl_add_u64 v[180:181], s[6:7], 0, v[184:185]
	v_lshl_add_u64 v[182:183], s[8:9], 0, v[184:185]
	v_lshl_add_u64 v[184:185], s[12:13], 0, v[184:185]
	v_lshl_add_u64 v[186:187], s[6:7], 0, v[132:133]
	v_lshl_add_u64 v[188:189], s[8:9], 0, v[132:133]
	v_lshl_add_u64 v[190:191], s[12:13], 0, v[132:133]
	s_lshl_b32 s36, s97, 4
	s_lshl_b32 s37, s33, 4
	v_or3_b32 v192, s3, v192, 3
	s_lshl_b32 s38, s33, 6
	v_add_u32_e32 v239, v131, v130
	v_and_b32_e32 v251, 63, v0
	v_lshlrev_b32_e32 v251, 4, v251
	v_add_u32_e32 v251, 0x18000, v251
	s_cmp_eq_u32 s96, 0
	s_cbranch_scc0 .Lp8_stage_1
	s_mov_b32 m0, 0x18000
	s_nop 0
	global_load_lds_dwordx4 v[144:145], off
	s_mov_b32 m0, 0x18400
	s_nop 0
	global_load_lds_dwordx4 v[146:147], off
	s_mov_b32 m0, 0x18800
	s_nop 0
	global_load_lds_dwordx4 v[148:149], off
	s_branch .Lp8_stage_done
.Lp8_stage_1:
	s_cmp_eq_u32 s96, 1
	s_cbranch_scc0 .Lp8_stage_2
	s_mov_b32 m0, 0x18800
	s_nop 0
	global_load_lds_dwordx4 v[144:145], off offset:1024
	s_mov_b32 m0, 0x19000
	s_nop 0
	global_load_lds_dwordx4 v[150:151], off
	s_mov_b32 m0, 0x19400
	s_nop 0
	global_load_lds_dwordx4 v[152:153], off
	s_branch .Lp8_stage_done
.Lp8_stage_2:
	s_cmp_eq_u32 s96, 2
	s_cbranch_scc0 .Lp8_stage_3
	s_mov_b32 m0, 0x19000
	s_nop 0
	global_load_lds_dwordx4 v[144:145], off offset:2048
	s_mov_b32 m0, 0x19c00
	s_nop 0
	global_load_lds_dwordx4 v[154:155], off
	s_mov_b32 m0, 0x1a000
	s_nop 0
	global_load_lds_dwordx4 v[156:157], off
	s_branch .Lp8_stage_done
.Lp8_stage_3:
	s_cmp_eq_u32 s96, 3
	s_cbranch_scc0 .Lp8_stage_4
	s_mov_b32 m0, 0x19800
	s_nop 0
	global_load_lds_dwordx4 v[144:145], off offset:3072
	s_mov_b32 m0, 0x1a800
	s_nop 0
	global_load_lds_dwordx4 v[158:159], off
	s_mov_b32 m0, 0x1ac00
	s_nop 0
	global_load_lds_dwordx4 v[160:161], off
	s_branch .Lp8_stage_done
.Lp8_stage_4:
	s_cmp_eq_u32 s96, 4
	s_cbranch_scc0 .Lp8_stage_5
	s_mov_b32 m0, 0x1b000
	s_nop 0
	global_load_lds_dwordx4 v[168:169], off
	s_mov_b32 m0, 0x1b400
	s_nop 0
	global_load_lds_dwordx4 v[170:171], off
	s_mov_b32 m0, 0x1b800
	s_nop 0
	global_load_lds_dwordx4 v[172:173], off
	s_branch .Lp8_stage_done
.Lp8_stage_5:
	s_cmp_eq_u32 s96, 5
	s_cbranch_scc0 .Lp8_stage_6
	s_mov_b32 m0, 0x1bc00
	s_nop 0
	global_load_lds_dwordx4 v[174:175], off
	s_mov_b32 m0, 0x1c000
	s_nop 0
	global_load_lds_dwordx4 v[176:177], off
	s_mov_b32 m0, 0x1c400
	s_nop 0
	global_load_lds_dwordx4 v[178:179], off
	s_branch .Lp8_stage_done
.Lp8_stage_6:
	s_cmp_eq_u32 s96, 6
	s_cbranch_scc0 .Lp8_stage_7
	s_mov_b32 m0, 0x1c800
	s_nop 0
	global_load_lds_dwordx4 v[180:181], off
	s_mov_b32 m0, 0x1cc00
	s_nop 0
	global_load_lds_dwordx4 v[182:183], off
	s_mov_b32 m0, 0x1d000
	s_nop 0
	global_load_lds_dwordx4 v[184:185], off
	s_branch .Lp8_stage_done
.Lp8_stage_7:
	s_mov_b32 m0, 0x1d400
	s_nop 0
	global_load_lds_dwordx4 v[186:187], off
	s_mov_b32 m0, 0x1d800
	s_nop 0
	global_load_lds_dwordx4 v[188:189], off
	s_mov_b32 m0, 0x1dc00
	s_nop 0
	global_load_lds_dwordx4 v[190:191], off
.Lp8_stage_done:
	s_waitcnt vmcnt(0)
	s_barrier
	s_branch .LBB0_1863

; DI float bflo(unsigned w) { return __uint_as_float(w << 16); }
; DI float bfhi(unsigned w) { return __uint_as_float(w & 0xffff0000u); }
; __global__ void __launch_bounds__(NWAVES * 64, 2) fwd_kernel(Args a_unused) {
;     ...
;             for (int q = 0; q < 2; ++q) { const int m = row0 + 2 * wave + q; const unsigned short* xr = X1 + (size_t)m * D + 4 * lane; f32x4 v[8]; float ss = 0.f;
; #pragma unroll
;                 for (int j = 0; j < 8; ++j) { const u32x2 w2 = *(const u32x2*)(xr + 256 * j); v[j] = (f32x4){bflo(w2[0]), bfhi(w2[0]), bflo(w2[1]), bfhi(w2[1])}; ss += v[j][0] * v[j][0] + v[j][1] * v[j][1] + v[j][2] * v[j][2] + v[j][3] * v[j][3]; }
;                 const float rstd = rsqrtf(wave_sum(ss) * (1.0f / D) + EPS);
;                 if (lane == 0) rsd[2 * wave + q] = rstd;
;                 float am = 0.f;
; #pragma unroll
;                 for (int j = 0; j < 8; ++j) { const int k = 4 * lane + 256 * j; const f32x4 g = *(const f32x4*)(A->norm_ffn_g + k), s1 = *(const f32x4*)(modl + 4 * 2048 + k), s0 = *(const f32x4*)(modl + 3 * 2048 + k);
;                     v[j] = v[j] * rstd * (g * (1.0f + s1)) + s0; am = fmaxf(am, fmaxf(fmaxf(fabsf(v[j][0]), fabsf(v[j][1])), fmaxf(fabsf(v[j][2]), fabsf(v[j][3])))); }
.LBB0_1863:
	s_add_i32 s6, s30, s36
	s_ashr_i32 s7, s6, 31
	s_lshl_b64 s[8:9], s[6:7], 12
	v_lshl_add_u64 v[130:131], v[134:135], 0, s[8:9]
	global_load_dwordx2 v[132:133], v[130:131], off
	global_load_dwordx2 v[194:195], v[130:131], off offset:512
	global_load_dwordx2 v[196:197], v[130:131], off offset:1024
	global_load_dwordx2 v[198:199], v[130:131], off offset:1536
	global_load_dwordx2 v[200:201], v[130:131], off offset:2560
	global_load_dwordx2 v[220:221], v[130:131], off offset:2048
	global_load_dwordx2 v[222:223], v[130:131], off offset:3584
	global_load_dwordx2 v[228:229], v[130:131], off offset:3072
	s_waitcnt vmcnt(7)
	v_and_b32_e32 v203, 0xffff0000, v132
	s_waitcnt vmcnt(6)
	v_and_b32_e32 v209, 0xffff0000, v194
	v_lshlrev_b32_e32 v202, 16, v132
	v_lshlrev_b32_e32 v208, 16, v194
	s_waitcnt vmcnt(5)
	v_and_b32_e32 v213, 0xffff0000, v196
	v_mul_f32_e32 v193, v203, v203
	v_mul_f32_e32 v206, v209, v209
	v_lshlrev_b32_e32 v204, 16, v133
	v_lshlrev_b32_e32 v210, 16, v195
	v_lshlrev_b32_e32 v212, 16, v196
	s_waitcnt vmcnt(4)
	v_and_b32_e32 v217, 0xffff0000, v198
	s_waitcnt vmcnt(0)
	v_lshlrev_b32_e32 v194, 16, v228
	v_and_b32_e32 v196, 0xffff0000, v228
	v_mul_f32_e32 v228, v213, v213
	v_fmac_f32_e32 v193, v202, v202
	v_fmac_f32_e32 v206, v208, v208
	v_and_b32_e32 v205, 0xffff0000, v133
	v_and_b32_e32 v211, 0xffff0000, v195
	v_lshlrev_b32_e32 v214, 16, v197
	v_lshlrev_b32_e32 v216, 16, v198
	v_lshlrev_b32_e32 v131, 16, v200
	v_and_b32_e32 v133, 0xffff0000, v200
	v_and_b32_e32 v132, 0xffff0000, v220
	v_lshlrev_b32_e32 v198, 16, v229
	v_and_b32_e32 v200, 0xffff0000, v229
	v_mul_f32_e32 v229, v217, v217
	v_fmac_f32_e32 v228, v212, v212
	v_fmac_f32_e32 v193, v204, v204
	v_fmac_f32_e32 v206, v210, v210
	v_and_b32_e32 v215, 0xffff0000, v197
	v_lshlrev_b32_e32 v218, 16, v199
	v_lshlrev_b32_e32 v130, 16, v220
	v_lshlrev_b32_e32 v224, 16, v221
	v_and_b32_e32 v226, 0xffff0000, v221
	v_pk_mul_f32 v[220:221], v[132:133], v[132:133]
	v_fmac_f32_e32 v229, v216, v216
	v_fmac_f32_e32 v228, v214, v214
	v_fmac_f32_e32 v193, v205, v205
	v_fmac_f32_e32 v206, v211, v211
	v_and_b32_e32 v219, 0xffff0000, v199
	v_lshlrev_b32_e32 v225, 16, v201
	v_and_b32_e32 v197, 0xffff0000, v222
	v_pk_fma_f32 v[220:221], v[130:131], v[130:131], v[220:221]
	v_fmac_f32_e32 v229, v218, v218
	v_fmac_f32_e32 v228, v215, v215
	v_add_f32_e32 v193, v193, v206
	v_and_b32_e32 v227, 0xffff0000, v201
	v_lshlrev_b32_e32 v195, 16, v222
	v_lshlrev_b32_e32 v199, 16, v223
	v_and_b32_e32 v201, 0xffff0000, v223
	v_pk_mul_f32 v[222:223], v[196:197], v[196:197]
	v_pk_fma_f32 v[220:221], v[224:225], v[224:225], v[220:221]
	v_fmac_f32_e32 v229, v219, v219
	v_add_f32_e32 v193, v193, v228
	v_pk_fma_f32 v[222:223], v[194:195], v[194:195], v[222:223]
	v_pk_fma_f32 v[220:221], v[226:227], v[226:227], v[220:221]
	v_add_f32_e32 v193, v193, v229
	v_pk_fma_f32 v[222:223], v[198:199], v[198:199], v[222:223]
	v_add_f32_e32 v193, v193, v220
	v_pk_fma_f32 v[222:223], v[200:201], v[200:201], v[222:223]
	v_add_f32_e32 v193, v193, v221
	v_add_f32_e32 v193, v193, v222
	v_add_f32_e32 v193, v193, v223
	s_waitcnt lgkmcnt(0)
	s_nop 1
	v_add_f32_dpp v193, v193, v193 quad_perm:[1,0,3,2] row_mask:0xf bank_mask:0xf
	s_nop 1
	v_add_f32_dpp v193, v193, v193 quad_perm:[2,3,0,1] row_mask:0xf bank_mask:0xf
	s_nop 1
	v_add_f32_dpp v193, v193, v193 row_half_mirror row_mask:0xf bank_mask:0xf
	s_nop 1
	v_add_f32_dpp v193, v193, v193 row_mirror row_mask:0xf bank_mask:0xf
	v_mov_b32_e32 v206, v193
	s_nop 1
	v_permlane16_swap_b32 v193, v206
	v_add_f32_e32 v193, v193, v206
	v_mov_b32_e32 v206, v193
	s_nop 1
	v_permlane32_swap_b32 v193, v206
	v_add_f32_e32 v193, v193, v206
	v_fmamk_f32 v193, v193, 0x3a000000, v238
	v_mul_f32_e32 v206, 0x4b800000, v193
	v_cmp_gt_f32_e32 vcc, s39, v193
	s_nop 1
	v_cndmask_b32_e32 v193, v193, v206, vcc
	v_rsq_f32_e32 v193, v193
	s_nop 0
	v_mul_f32_e32 v206, 0x45800000, v193
	v_cndmask_b32_e32 v206, v193, v206, vcc
	s_and_saveexec_b64 s[8:9], s[4:5]
	v_mov_b32_e32 v193, s31
	ds_write_b32 v193, v206 offset:16384
	s_or_b64 exec, exec, s[8:9]
	ds_read_b128 v[220:223], v251 offset:0
	ds_read_b128 v[228:231], v251 offset:1024
	ds_read_b128 v[242:245], v251 offset:2048
	v_pk_mul_f32 v[246:247], v[206:207], v[202:203] op_sel_hi:[0,1]
	v_pk_mul_f32 v[202:203], v[206:207], v[204:205] op_sel_hi:[0,1]
	v_mov_b32_e32 v249, v226
	v_mov_b32_e32 v226, v225
	s_waitcnt lgkmcnt(1)
	v_pk_add_f32 v[204:205], v[230:231], 1.0 op_sel_hi:[1,0]
	v_pk_add_f32 v[228:229], v[228:229], 1.0 op_sel_hi:[1,0]
	v_pk_mul_f32 v[204:205], v[222:223], v[204:205]
	v_pk_mul_f32 v[220:221], v[220:221], v[228:229]
	s_waitcnt lgkmcnt(0)
	v_pk_fma_f32 v[202:203], v[204:205], v[202:203], v[244:245]
	v_pk_fma_f32 v[204:205], v[220:221], v[246:247], v[242:243]
	ds_read_b128 v[220:223], v251 offset:3072
	ds_read_b128 v[228:231], v251 offset:4096
	ds_read_b128 v[242:245], v251 offset:5120
	v_pk_mul_f32 v[246:247], v[206:207], v[208:209] op_sel_hi:[0,1]
	v_pk_mul_f32 v[208:209], v[206:207], v[210:211] op_sel_hi:[0,1]
	v_max_f32_e64 v193, |v202|, |v203|
	v_max3_f32 v193, |v204|, |v205|, v193
	s_waitcnt lgkmcnt(1)
	v_pk_add_f32 v[210:211], v[230:231], 1.0 op_sel_hi:[1,0]
	v_pk_add_f32 v[228:229], v[228:229], 1.0 op_sel_hi:[1,0]
	v_pk_mul_f32 v[210:211], v[222:223], v[210:211]
	v_pk_mul_f32 v[220:221], v[220:221], v[228:229]
	s_waitcnt lgkmcnt(0)
	v_pk_fma_f32 v[208:209], v[210:211], v[208:209], v[244:245]
	v_pk_fma_f32 v[210:211], v[220:221], v[246:247], v[242:243]
	v_max_f32_e64 v220, |v208|, |v209|
	v_max3_f32 v220, |v210|, |v211|, v220
	v_max3_f32 v193, v193, 0, v220
	ds_read_b128 v[220:223], v251 offset:6144
	ds_read_b128 v[228:231], v251 offset:7168
	ds_read_b128 v[242:245], v251 offset:8192
	v_pk_mul_f32 v[246:247], v[206:207], v[212:213] op_sel_hi:[0,1]
	v_pk_mul_f32 v[212:213], v[206:207], v[214:215] op_sel_hi:[0,1]
	s_waitcnt lgkmcnt(1)
; __global__ void __launch_bounds__(NWAVES * 64, 2) fwd_kernel(Args a_unused) {
;     ...
;                 float am = 0.f;
; #pragma unroll
;                 for (int j = 0; j < 8; ++j) { const int k = 4 * lane + 256 * j; const f32x4 g = *(const f32x4*)(A->norm_ffn_g + k), s1 = *(const f32x4*)(modl + 4 * 2048 + k), s0 = *(const f32x4*)(modl + 3 * 2048 + k);
;                     v[j] = v[j] * rstd * (g * (1.0f + s1)) + s0; am = fmaxf(am, fmaxf(fmaxf(fabsf(v[j][0]), fabsf(v[j][1])), fmaxf(fabsf(v[j][2]), fabsf(v[j][3])))); }
; #pragma unroll
;                 for (int o = 1; o < 64; o <<= 1) am = fmaxf(am, __shfl_xor(am, o));
;                 if (am == 0.f) am = 1.f;
;                 const float qi = 127.0f / am;
;                 if (lane == 0) ((float*)(ws + WS_CS + CS_ROW))[m] = am * (1.0f / 127.0f);
	v_pk_add_f32 v[214:215], v[230:231], 1.0 op_sel_hi:[1,0]
	v_pk_add_f32 v[228:229], v[228:229], 1.0 op_sel_hi:[1,0]
	v_pk_mul_f32 v[214:215], v[222:223], v[214:215]
	v_pk_mul_f32 v[220:221], v[220:221], v[228:229]
	s_waitcnt lgkmcnt(0)
	v_pk_fma_f32 v[212:213], v[214:215], v[212:213], v[244:245]
	v_pk_fma_f32 v[214:215], v[220:221], v[246:247], v[242:243]
	v_max_f32_e64 v220, |v212|, |v213|
	v_max3_f32 v248, |v214|, |v215|, v220
	ds_read_b128 v[220:223], v251 offset:9216
	ds_read_b128 v[228:231], v251 offset:10240
	ds_read_b128 v[242:245], v251 offset:11264
	v_pk_mul_f32 v[246:247], v[206:207], v[216:217] op_sel_hi:[0,1]
	v_pk_mul_f32 v[216:217], v[206:207], v[218:219] op_sel_hi:[0,1]
	s_waitcnt lgkmcnt(1)
	v_pk_add_f32 v[218:219], v[230:231], 1.0 op_sel_hi:[1,0]
	v_pk_add_f32 v[228:229], v[228:229], 1.0 op_sel_hi:[1,0]
	v_pk_mul_f32 v[218:219], v[222:223], v[218:219]
	v_pk_mul_f32 v[220:221], v[220:221], v[228:229]
	s_waitcnt lgkmcnt(0)
	v_pk_fma_f32 v[216:217], v[218:219], v[216:217], v[244:245]
	v_pk_fma_f32 v[218:219], v[220:221], v[246:247], v[242:243]
	v_max_f32_e64 v220, |v216|, |v217|
	v_max3_f32 v220, |v218|, |v219|, v220
	v_max3_f32 v193, v193, v248, v220
	ds_read_b128 v[220:223], v251 offset:12288
	ds_read_b128 v[228:231], v251 offset:13312
	ds_read_b128 v[242:245], v251 offset:14336
	v_mov_b32_e32 v246, v130
	v_mov_b32_e32 v247, v132
	v_mov_b32_e32 v248, v224
	v_pk_mul_f32 v[246:247], v[206:207], v[246:247] op_sel_hi:[0,1]
	v_pk_mul_f32 v[248:249], v[206:207], v[248:249] op_sel_hi:[0,1]
	v_mov_b32_e32 v132, v131
	s_waitcnt lgkmcnt(1)
	v_pk_add_f32 v[230:231], v[230:231], 1.0 op_sel_hi:[1,0]
	v_pk_add_f32 v[228:229], v[228:229], 1.0 op_sel_hi:[1,0]
	v_pk_mul_f32 v[222:223], v[222:223], v[230:231]
	v_pk_mul_f32 v[228:229], v[220:221], v[228:229]
	s_waitcnt lgkmcnt(0)
	v_pk_fma_f32 v[220:221], v[222:223], v[248:249], v[244:245]
	v_pk_fma_f32 v[222:223], v[228:229], v[246:247], v[242:243]
	ds_read_b128 v[228:231], v251 offset:15360
	ds_read_b128 v[242:245], v251 offset:16384
	ds_read_b128 v[246:249], v251 offset:17408
	v_max_f32_e64 v130, |v220|, |v221|
	v_max3_f32 v250, |v222|, |v223|, v130
	v_pk_mul_f32 v[130:131], v[206:207], v[132:133] op_sel_hi:[0,1]
	v_pk_mul_f32 v[132:133], v[206:207], v[226:227] op_sel_hi:[0,1]
	s_waitcnt lgkmcnt(1)
	v_pk_add_f32 v[224:225], v[244:245], 1.0 op_sel_hi:[1,0]
	v_pk_add_f32 v[226:227], v[242:243], 1.0 op_sel_hi:[1,0]
	v_pk_mul_f32 v[224:225], v[230:231], v[224:225]
	v_pk_mul_f32 v[226:227], v[228:229], v[226:227]
	s_waitcnt lgkmcnt(0)
	v_pk_fma_f32 v[224:225], v[224:225], v[132:133], v[248:249]
	v_pk_fma_f32 v[226:227], v[226:227], v[130:131], v[246:247]
	v_max_f32_e64 v130, |v224|, |v225|
	v_max3_f32 v130, |v226|, |v227|, v130
	v_max3_f32 v193, v193, v250, v130
	ds_read_b128 v[130:133], v251 offset:18432
	ds_read_b128 v[228:231], v251 offset:19456
	ds_read_b128 v[242:245], v251 offset:20480
	v_mov_b32_e32 v248, v198
	v_mov_b32_e32 v249, v200
	v_mov_b32_e32 v246, v194
	v_mov_b32_e32 v247, v196
	v_pk_mul_f32 v[248:249], v[206:207], v[248:249] op_sel_hi:[0,1]
	v_pk_mul_f32 v[246:247], v[206:207], v[246:247] op_sel_hi:[0,1]
	v_mov_b32_e32 v196, v195
	v_mov_b32_e32 v200, v199
	v_pk_mul_f32 v[194:195], v[206:207], v[196:197] op_sel_hi:[0,1]
	v_pk_mul_f32 v[196:197], v[206:207], v[200:201] op_sel_hi:[0,1]
	s_waitcnt lgkmcnt(1)
	v_pk_add_f32 v[230:231], v[230:231], 1.0 op_sel_hi:[1,0]
	v_pk_add_f32 v[228:229], v[228:229], 1.0 op_sel_hi:[1,0]
	v_pk_mul_f32 v[132:133], v[132:133], v[230:231]
	v_pk_mul_f32 v[130:131], v[130:131], v[228:229]
	s_waitcnt lgkmcnt(0)
	v_pk_fma_f32 v[228:229], v[132:133], v[248:249], v[244:245]
	v_pk_fma_f32 v[230:231], v[130:131], v[246:247], v[242:243]
	v_max_f32_e64 v130, |v228|, |v229|
	v_max3_f32 v250, |v230|, |v231|, v130
	ds_read_b128 v[130:133], v251 offset:21504
	ds_read_b128 v[242:245], v251 offset:22528
	ds_read_b128 v[246:249], v251 offset:23552
	s_waitcnt lgkmcnt(1)
	v_pk_add_f32 v[198:199], v[244:245], 1.0 op_sel_hi:[1,0]
	v_pk_add_f32 v[200:201], v[242:243], 1.0 op_sel_hi:[1,0]
	v_pk_mul_f32 v[132:133], v[132:133], v[198:199]
	v_pk_mul_f32 v[198:199], v[130:131], v[200:201]
	s_waitcnt lgkmcnt(0)
	v_pk_fma_f32 v[130:131], v[132:133], v[196:197], v[248:249]
	v_pk_fma_f32 v[132:133], v[198:199], v[194:195], v[246:247]
	v_max_f32_e64 v194, |v130|, |v131|
	v_max3_f32 v194, |v132|, |v133|, v194
	v_max3_f32 v193, v193, v250, v194
	s_waitcnt lgkmcnt(0)
	s_nop 1
	v_max_f32_dpp v193, v193, v193 quad_perm:[1,0,3,2] row_mask:0xf bank_mask:0xf
	s_nop 1
	v_max_f32_dpp v193, v193, v193 quad_perm:[2,3,0,1] row_mask:0xf bank_mask:0xf
	s_nop 1
	v_max_f32_dpp v193, v193, v193 row_half_mirror row_mask:0xf bank_mask:0xf
	s_nop 1
	v_max_f32_dpp v193, v193, v193 row_mirror row_mask:0xf bank_mask:0xf
	v_mov_b32_e32 v194, v193
	s_nop 1
	v_permlane16_swap_b32 v193, v194
	v_max_f32_e32 v193, v193, v194
	v_mov_b32_e32 v194, v193
	s_nop 1
	v_permlane32_swap_b32 v193, v194
	v_max_f32_e32 v193, v193, v194
	v_cmp_neq_f32_e32 vcc, 0, v193
	s_nop 1
	v_cndmask_b32_e32 v193, 1.0, v193, vcc
	s_and_saveexec_b64 s[8:9], s[4:5]
	s_cbranch_execz .LBB0_1867
	s_lshl_b64 s[10:11], s[6:7], 2
	s_add_u32 s10, s34, s10
	s_addc_u32 s11, s35, s11
	v_mul_f32_e32 v194, 0x3c010204, v193
	global_store_dword v165, v194, s[10:11]
; DI float bflo(unsigned w) { return __uint_as_float(w << 16); }
; DI float bfhi(unsigned w) { return __uint_as_float(w & 0xffff0000u); }
; __global__ void __launch_bounds__(NWAVES * 64, 2) fwd_kernel(Args a_unused) {
;     ...
;             for (int q = 0; q < 2; ++q) { const int m = row0 + 2 * wave + q; const unsigned short* xr = X1 + (size_t)m * D + 4 * lane; f32x4 v[8]; float ss = 0.f;
; #pragma unroll
;                 for (int j = 0; j < 8; ++j) { const u32x2 w2 = *(const u32x2*)(xr + 256 * j); v[j] = (f32x4){bflo(w2[0]), bfhi(w2[0]), bflo(w2[1]), bfhi(w2[1])}; ss += v[j][0] * v[j][0] + v[j][1] * v[j][1] + v[j][2] * v[j][2] + v[j][3] * v[j][3]; }
;     ...
;                 const float qi = 127.0f / am;
;                 if (lane == 0) ((float*)(ws + WS_CS + CS_ROW))[m] = am * (1.0f / 127.0f);
;                 unsigned* hq = (unsigned*)((signed char*)(ws + WS_H) + (size_t)m * D + 4 * lane);
; #pragma unroll
;                 for (int j = 0; j < 8; ++j) hq[64 * j] = q8x4(v[j][0], v[j][1], v[j][2], v[j][3], qi); }
.LBB0_1867:
	s_or_b64 exec, exec, s[8:9]
	v_div_scale_f32 v194, s[8:9], v193, v193, s42
	v_rcp_f32_e32 v195, v194
	s_lshl_b64 s[8:9], s[6:7], 11
	s_add_i32 s6, s6, 1
	s_ashr_i32 s7, s6, 31
	v_fma_f32 v196, -v194, v195, 1.0
	v_fmac_f32_e32 v195, v196, v195
	v_div_scale_f32 v196, vcc, s42, v193, s42
	v_mul_f32_e32 v197, v196, v195
	v_fma_f32 v198, -v194, v197, v196
	v_fmac_f32_e32 v197, v198, v195
	v_fma_f32 v194, -v194, v197, v196
	v_div_fmas_f32 v194, v194, v195, v197
	v_div_fixup_f32 v193, v194, v193, s42
	v_fmaak_f32 v196, v204, v193, 0x4b400000
	v_fmaak_f32 v197, v205, v193, 0x4b400000
	v_fmaak_f32 v198, v202, v193, 0x4b400000
	v_fmaak_f32 v199, v203, v193, 0x4b400000
	v_perm_b32 v198, v199, v198, s43
	v_perm_b32 v196, v197, v196, s43
	v_lshl_add_u64 v[194:195], v[136:137], 0, s[8:9]
	v_perm_b32 v196, v198, v196, s44
	global_store_dword v[194:195], v196, off
	v_fmaak_f32 v196, v210, v193, 0x4b400000
	v_fmaak_f32 v197, v211, v193, 0x4b400000
	v_fmaak_f32 v198, v208, v193, 0x4b400000
	v_fmaak_f32 v199, v209, v193, 0x4b400000
	v_perm_b32 v198, v199, v198, s43
	v_perm_b32 v196, v197, v196, s43
	v_perm_b32 v196, v198, v196, s44
	global_store_dword v[194:195], v196, off offset:256
	v_fmaak_f32 v196, v214, v193, 0x4b400000
	v_fmaak_f32 v197, v215, v193, 0x4b400000
	v_fmaak_f32 v198, v212, v193, 0x4b400000
	v_fmaak_f32 v199, v213, v193, 0x4b400000
	v_perm_b32 v198, v199, v198, s43
	v_perm_b32 v196, v197, v196, s43
	v_perm_b32 v196, v198, v196, s44
	global_store_dword v[194:195], v196, off offset:512
	v_fmaak_f32 v196, v218, v193, 0x4b400000
	v_fmaak_f32 v197, v219, v193, 0x4b400000
	v_fmaak_f32 v198, v216, v193, 0x4b400000
	v_fmaak_f32 v199, v217, v193, 0x4b400000
	v_perm_b32 v198, v199, v198, s43
	v_perm_b32 v196, v197, v196, s43
	v_perm_b32 v196, v198, v196, s44
	global_store_dword v[194:195], v196, off offset:768
	v_fmaak_f32 v196, v222, v193, 0x4b400000
	v_fmaak_f32 v197, v223, v193, 0x4b400000
	v_fmaak_f32 v198, v220, v193, 0x4b400000
	v_fmaak_f32 v199, v221, v193, 0x4b400000
	v_perm_b32 v198, v199, v198, s43
	v_perm_b32 v196, v197, v196, s43
	v_perm_b32 v196, v198, v196, s44
	global_store_dword v[194:195], v196, off offset:1024
	v_fmaak_f32 v196, v226, v193, 0x4b400000
	v_fmaak_f32 v197, v227, v193, 0x4b400000
	v_fmaak_f32 v198, v224, v193, 0x4b400000
	v_fmaak_f32 v199, v225, v193, 0x4b400000
	v_perm_b32 v198, v199, v198, s43
	v_perm_b32 v196, v197, v196, s43
	v_perm_b32 v196, v198, v196, s44
	global_store_dword v[194:195], v196, off offset:1280
	v_fmaak_f32 v196, v230, v193, 0x4b400000
	v_fmaak_f32 v197, v231, v193, 0x4b400000
	v_fmaak_f32 v198, v228, v193, 0x4b400000
	v_fmaak_f32 v199, v229, v193, 0x4b400000
	v_fmaak_f32 v132, v132, v193, 0x4b400000
	v_fmaak_f32 v133, v133, v193, 0x4b400000
	v_fmaak_f32 v130, v130, v193, 0x4b400000
	v_fmaak_f32 v131, v131, v193, 0x4b400000
	v_perm_b32 v198, v199, v198, s43
	v_perm_b32 v196, v197, v196, s43
	v_perm_b32 v130, v131, v130, s43
	v_perm_b32 v131, v133, v132, s43
	v_perm_b32 v196, v198, v196, s44
	v_perm_b32 v130, v130, v131, s44
	s_lshl_b64 s[8:9], s[6:7], 12
	global_store_dword v[194:195], v196, off offset:1536
	global_store_dword v[194:195], v130, off offset:1792
	v_lshl_add_u64 v[130:131], v[134:135], 0, s[8:9]
	global_load_dwordx2 v[132:133], v[130:131], off
	global_load_dwordx2 v[198:199], v[130:131], off offset:512
	global_load_dwordx2 v[200:201], v[130:131], off offset:1024
	global_load_dwordx2 v[202:203], v[130:131], off offset:1536
	global_load_dwordx2 v[204:205], v[130:131], off offset:2560
	global_load_dwordx2 v[220:221], v[130:131], off offset:2048
	global_load_dwordx2 v[222:223], v[130:131], off offset:3584
	global_load_dwordx2 v[228:229], v[130:131], off offset:3072
	s_waitcnt vmcnt(7)
	v_and_b32_e32 v195, 0xffff0000, v132
	s_waitcnt vmcnt(6)
	v_and_b32_e32 v209, 0xffff0000, v198
	v_lshlrev_b32_e32 v194, 16, v132
	v_lshlrev_b32_e32 v208, 16, v198
	v_mul_f32_e32 v130, v195, v195
	v_mul_f32_e32 v131, v209, v209
	v_lshlrev_b32_e32 v196, 16, v133
	v_fmac_f32_e32 v130, v194, v194
	v_lshlrev_b32_e32 v210, 16, v199
	v_fmac_f32_e32 v131, v208, v208
	v_and_b32_e32 v197, 0xffff0000, v133
	v_fmac_f32_e32 v130, v196, v196
	v_and_b32_e32 v211, 0xffff0000, v199
	v_fmac_f32_e32 v131, v210, v210
	v_fmac_f32_e32 v130, v197, v197
	v_fmac_f32_e32 v131, v211, v211
	s_waitcnt vmcnt(5)
	v_and_b32_e32 v213, 0xffff0000, v200
	v_add_f32_e32 v130, v130, v131
	v_lshlrev_b32_e32 v212, 16, v200
	v_mul_f32_e32 v131, v213, v213
	v_lshlrev_b32_e32 v214, 16, v201
	v_fmac_f32_e32 v131, v212, v212
	v_and_b32_e32 v215, 0xffff0000, v201
	v_fmac_f32_e32 v131, v214, v214
	v_fmac_f32_e32 v131, v215, v215
	s_waitcnt vmcnt(4)
	v_and_b32_e32 v217, 0xffff0000, v202
	v_add_f32_e32 v130, v130, v131
	v_lshlrev_b32_e32 v216, 16, v202
	v_mul_f32_e32 v131, v217, v217
	v_lshlrev_b32_e32 v218, 16, v203
	v_fmac_f32_e32 v131, v216, v216
	v_and_b32_e32 v219, 0xffff0000, v203
	v_fmac_f32_e32 v131, v218, v218
	v_fmac_f32_e32 v131, v219, v219
	s_waitcnt vmcnt(3)
	v_and_b32_e32 v133, 0xffff0000, v204
	s_waitcnt vmcnt(2)
	v_and_b32_e32 v132, 0xffff0000, v220
	v_add_f32_e32 v193, v130, v131
	v_lshlrev_b32_e32 v131, 16, v204
	v_lshlrev_b32_e32 v130, 16, v220
	v_pk_mul_f32 v[198:199], v[132:133], v[132:133]
	v_lshlrev_b32_e32 v225, 16, v205
	v_lshlrev_b32_e32 v224, 16, v221
	v_pk_fma_f32 v[198:199], v[130:131], v[130:131], v[198:199]
	v_and_b32_e32 v227, 0xffff0000, v205
	v_and_b32_e32 v226, 0xffff0000, v221
	v_pk_fma_f32 v[198:199], v[224:225], v[224:225], v[198:199]
	s_waitcnt vmcnt(1)
	v_and_b32_e32 v201, 0xffff0000, v222
	v_pk_fma_f32 v[198:199], v[226:227], v[226:227], v[198:199]
	s_waitcnt vmcnt(0)
; DI float bflo(unsigned w) { return __uint_as_float(w << 16); }
; DI float bfhi(unsigned w) { return __uint_as_float(w & 0xffff0000u); }
; __global__ void __launch_bounds__(NWAVES * 64, 2) fwd_kernel(Args a_unused) {
;     ...
;                 for (int j = 0; j < 8; ++j) { const u32x2 w2 = *(const u32x2*)(xr + 256 * j); v[j] = (f32x4){bflo(w2[0]), bfhi(w2[0]), bflo(w2[1]), bfhi(w2[1])}; ss += v[j][0] * v[j][0] + v[j][1] * v[j][1] + v[j][2] * v[j][2] + v[j][3] * v[j][3]; }
;                 const float rstd = rsqrtf(wave_sum(ss) * (1.0f / D) + EPS);
;                 if (lane == 0) rsd[2 * wave + q] = rstd;
;                 float am = 0.f;
; #pragma unroll
;                 for (int j = 0; j < 8; ++j) { const int k = 4 * lane + 256 * j; const f32x4 g = *(const f32x4*)(A->norm_ffn_g + k), s1 = *(const f32x4*)(modl + 4 * 2048 + k), s0 = *(const f32x4*)(modl + 3 * 2048 + k);
;                     v[j] = v[j] * rstd * (g * (1.0f + s1)) + s0; am = fmaxf(am, fmaxf(fmaxf(fabsf(v[j][0]), fabsf(v[j][1])), fmaxf(fabsf(v[j][2]), fabsf(v[j][3])))); }
	v_and_b32_e32 v200, 0xffff0000, v228
	v_add_f32_e32 v193, v193, v198
	v_add_f32_e32 v193, v193, v199
	v_lshlrev_b32_e32 v199, 16, v222
	v_lshlrev_b32_e32 v198, 16, v228
	v_pk_mul_f32 v[220:221], v[200:201], v[200:201]
	v_lshlrev_b32_e32 v203, 16, v223
	v_lshlrev_b32_e32 v202, 16, v229
	v_pk_fma_f32 v[220:221], v[198:199], v[198:199], v[220:221]
	v_and_b32_e32 v205, 0xffff0000, v223
	v_and_b32_e32 v204, 0xffff0000, v229
	v_pk_fma_f32 v[220:221], v[202:203], v[202:203], v[220:221]
	s_nop 0
	v_pk_fma_f32 v[220:221], v[204:205], v[204:205], v[220:221]
	s_nop 0
	v_add_f32_e32 v193, v193, v220
	v_add_f32_e32 v193, v193, v221
	s_waitcnt lgkmcnt(0)
	s_nop 1
	v_add_f32_dpp v193, v193, v193 quad_perm:[1,0,3,2] row_mask:0xf bank_mask:0xf
	s_nop 1
	v_add_f32_dpp v193, v193, v193 quad_perm:[2,3,0,1] row_mask:0xf bank_mask:0xf
	s_nop 1
	v_add_f32_dpp v193, v193, v193 row_half_mirror row_mask:0xf bank_mask:0xf
	s_nop 1
	v_add_f32_dpp v193, v193, v193 row_mirror row_mask:0xf bank_mask:0xf
	v_mov_b32_e32 v206, v193
	s_nop 1
	v_permlane16_swap_b32 v193, v206
	v_add_f32_e32 v193, v193, v206
	v_mov_b32_e32 v206, v193
	s_nop 1
	v_permlane32_swap_b32 v193, v206
	v_add_f32_e32 v193, v193, v206
	v_fmamk_f32 v193, v193, 0x3a000000, v238
	v_mul_f32_e32 v206, 0x4b800000, v193
	v_cmp_gt_f32_e32 vcc, s39, v193
	s_nop 1
	v_cndmask_b32_e32 v193, v193, v206, vcc
	v_rsq_f32_e32 v193, v193
	s_nop 0
	v_mul_f32_e32 v206, 0x45800000, v193
	v_cndmask_b32_e32 v206, v193, v206, vcc
	s_and_saveexec_b64 s[8:9], s[4:5]
	v_mov_b32_e32 v193, s31
	ds_write_b32 v193, v206 offset:16388
	s_or_b64 exec, exec, s[8:9]
	ds_read_b128 v[220:223], v251 offset:0
	ds_read_b128 v[228:231], v251 offset:1024
	ds_read_b128 v[242:245], v251 offset:2048
	v_pk_mul_f32 v[246:247], v[206:207], v[194:195] op_sel_hi:[0,1]
	v_pk_mul_f32 v[194:195], v[206:207], v[196:197] op_sel_hi:[0,1]
	v_mov_b32_e32 v249, v226
	v_mov_b32_e32 v226, v225
	s_waitcnt lgkmcnt(1)
	v_pk_add_f32 v[196:197], v[230:231], 1.0 op_sel_hi:[1,0]
	v_pk_add_f32 v[228:229], v[228:229], 1.0 op_sel_hi:[1,0]
	v_pk_mul_f32 v[196:197], v[222:223], v[196:197]
	v_pk_mul_f32 v[220:221], v[220:221], v[228:229]
	s_waitcnt lgkmcnt(0)
	v_pk_fma_f32 v[194:195], v[196:197], v[194:195], v[244:245]
	v_pk_fma_f32 v[196:197], v[220:221], v[246:247], v[242:243]
	ds_read_b128 v[220:223], v251 offset:3072
	ds_read_b128 v[228:231], v251 offset:4096
	ds_read_b128 v[242:245], v251 offset:5120
	v_pk_mul_f32 v[246:247], v[206:207], v[208:209] op_sel_hi:[0,1]
	v_pk_mul_f32 v[208:209], v[206:207], v[210:211] op_sel_hi:[0,1]
	v_max_f32_e64 v193, |v194|, |v195|
	v_max3_f32 v193, |v196|, |v197|, v193
	s_waitcnt lgkmcnt(1)
	v_pk_add_f32 v[210:211], v[230:231], 1.0 op_sel_hi:[1,0]
	v_pk_add_f32 v[228:229], v[228:229], 1.0 op_sel_hi:[1,0]
	v_pk_mul_f32 v[210:211], v[222:223], v[210:211]
	v_pk_mul_f32 v[220:221], v[220:221], v[228:229]
	s_waitcnt lgkmcnt(0)
	v_pk_fma_f32 v[208:209], v[210:211], v[208:209], v[244:245]
	v_pk_fma_f32 v[210:211], v[220:221], v[246:247], v[242:243]
	v_max_f32_e64 v220, |v208|, |v209|
	v_max3_f32 v220, |v210|, |v211|, v220
	v_max3_f32 v193, v193, 0, v220
	ds_read_b128 v[220:223], v251 offset:6144
	ds_read_b128 v[228:231], v251 offset:7168
	ds_read_b128 v[242:245], v251 offset:8192
	v_pk_mul_f32 v[246:247], v[206:207], v[212:213] op_sel_hi:[0,1]
	v_pk_mul_f32 v[212:213], v[206:207], v[214:215] op_sel_hi:[0,1]
	s_waitcnt lgkmcnt(1)
	v_pk_add_f32 v[214:215], v[230:231], 1.0 op_sel_hi:[1,0]
	v_pk_add_f32 v[228:229], v[228:229], 1.0 op_sel_hi:[1,0]
	v_pk_mul_f32 v[214:215], v[222:223], v[214:215]
	v_pk_mul_f32 v[220:221], v[220:221], v[228:229]
	s_waitcnt lgkmcnt(0)
	v_pk_fma_f32 v[212:213], v[214:215], v[212:213], v[244:245]
	v_pk_fma_f32 v[214:215], v[220:221], v[246:247], v[242:243]
	v_max_f32_e64 v220, |v212|, |v213|
	v_max3_f32 v248, |v214|, |v215|, v220
	ds_read_b128 v[220:223], v251 offset:9216
	ds_read_b128 v[228:231], v251 offset:10240
	ds_read_b128 v[242:245], v251 offset:11264
	v_pk_mul_f32 v[246:247], v[206:207], v[216:217] op_sel_hi:[0,1]
	v_pk_mul_f32 v[216:217], v[206:207], v[218:219] op_sel_hi:[0,1]
	s_waitcnt lgkmcnt(1)
	v_pk_add_f32 v[218:219], v[230:231], 1.0 op_sel_hi:[1,0]
	v_pk_add_f32 v[228:229], v[228:229], 1.0 op_sel_hi:[1,0]
	v_pk_mul_f32 v[218:219], v[222:223], v[218:219]
	v_pk_mul_f32 v[220:221], v[220:221], v[228:229]
	s_waitcnt lgkmcnt(0)
; __global__ void __launch_bounds__(NWAVES * 64, 2) fwd_kernel(Args a_unused) {
;     ...
;                 float am = 0.f;
; #pragma unroll
;                 for (int j = 0; j < 8; ++j) { const int k = 4 * lane + 256 * j; const f32x4 g = *(const f32x4*)(A->norm_ffn_g + k), s1 = *(const f32x4*)(modl + 4 * 2048 + k), s0 = *(const f32x4*)(modl + 3 * 2048 + k);
;                     v[j] = v[j] * rstd * (g * (1.0f + s1)) + s0; am = fmaxf(am, fmaxf(fmaxf(fabsf(v[j][0]), fabsf(v[j][1])), fmaxf(fabsf(v[j][2]), fabsf(v[j][3])))); }
; #pragma unroll
;                 for (int o = 1; o < 64; o <<= 1) am = fmaxf(am, __shfl_xor(am, o));
;                 if (am == 0.f) am = 1.f;
;                 const float qi = 127.0f / am;
;                 if (lane == 0) ((float*)(ws + WS_CS + CS_ROW))[m] = am * (1.0f / 127.0f);
	v_pk_fma_f32 v[216:217], v[218:219], v[216:217], v[244:245]
	v_pk_fma_f32 v[218:219], v[220:221], v[246:247], v[242:243]
	v_max_f32_e64 v220, |v216|, |v217|
	v_max3_f32 v220, |v218|, |v219|, v220
	v_max3_f32 v193, v193, v248, v220
	ds_read_b128 v[220:223], v251 offset:12288
	ds_read_b128 v[228:231], v251 offset:13312
	ds_read_b128 v[242:245], v251 offset:14336
	v_mov_b32_e32 v246, v130
	v_mov_b32_e32 v247, v132
	v_mov_b32_e32 v248, v224
	v_pk_mul_f32 v[246:247], v[206:207], v[246:247] op_sel_hi:[0,1]
	v_pk_mul_f32 v[248:249], v[206:207], v[248:249] op_sel_hi:[0,1]
	v_mov_b32_e32 v132, v131
	s_waitcnt lgkmcnt(1)
	v_pk_add_f32 v[230:231], v[230:231], 1.0 op_sel_hi:[1,0]
	v_pk_add_f32 v[228:229], v[228:229], 1.0 op_sel_hi:[1,0]
	v_pk_mul_f32 v[222:223], v[222:223], v[230:231]
	v_pk_mul_f32 v[228:229], v[220:221], v[228:229]
	s_waitcnt lgkmcnt(0)
	v_pk_fma_f32 v[220:221], v[222:223], v[248:249], v[244:245]
	v_pk_fma_f32 v[222:223], v[228:229], v[246:247], v[242:243]
	ds_read_b128 v[228:231], v251 offset:15360
	ds_read_b128 v[242:245], v251 offset:16384
	ds_read_b128 v[246:249], v251 offset:17408
	v_max_f32_e64 v130, |v220|, |v221|
	v_max3_f32 v250, |v222|, |v223|, v130
	v_pk_mul_f32 v[130:131], v[206:207], v[132:133] op_sel_hi:[0,1]
	v_pk_mul_f32 v[132:133], v[206:207], v[226:227] op_sel_hi:[0,1]
	s_waitcnt lgkmcnt(1)
	v_pk_add_f32 v[224:225], v[244:245], 1.0 op_sel_hi:[1,0]
	v_pk_add_f32 v[226:227], v[242:243], 1.0 op_sel_hi:[1,0]
	v_pk_mul_f32 v[224:225], v[230:231], v[224:225]
	v_pk_mul_f32 v[226:227], v[228:229], v[226:227]
	s_waitcnt lgkmcnt(0)
	v_pk_fma_f32 v[224:225], v[224:225], v[132:133], v[248:249]
	v_pk_fma_f32 v[226:227], v[226:227], v[130:131], v[246:247]
	v_max_f32_e64 v130, |v224|, |v225|
	v_max3_f32 v130, |v226|, |v227|, v130
	v_max3_f32 v193, v193, v250, v130
	ds_read_b128 v[130:133], v251 offset:18432
	ds_read_b128 v[228:231], v251 offset:19456
	ds_read_b128 v[242:245], v251 offset:20480
	v_mov_b32_e32 v248, v202
	v_mov_b32_e32 v249, v204
	v_mov_b32_e32 v246, v198
	v_mov_b32_e32 v247, v200
	v_pk_mul_f32 v[248:249], v[206:207], v[248:249] op_sel_hi:[0,1]
	v_pk_mul_f32 v[246:247], v[206:207], v[246:247] op_sel_hi:[0,1]
	v_mov_b32_e32 v200, v199
	v_mov_b32_e32 v204, v203
	v_pk_mul_f32 v[198:199], v[206:207], v[200:201] op_sel_hi:[0,1]
	v_pk_mul_f32 v[200:201], v[206:207], v[204:205] op_sel_hi:[0,1]
	s_waitcnt lgkmcnt(1)
	v_pk_add_f32 v[230:231], v[230:231], 1.0 op_sel_hi:[1,0]
	v_pk_add_f32 v[228:229], v[228:229], 1.0 op_sel_hi:[1,0]
	v_pk_mul_f32 v[132:133], v[132:133], v[230:231]
	v_pk_mul_f32 v[130:131], v[130:131], v[228:229]
	s_waitcnt lgkmcnt(0)
	v_pk_fma_f32 v[228:229], v[132:133], v[248:249], v[244:245]
	v_pk_fma_f32 v[230:231], v[130:131], v[246:247], v[242:243]
	v_max_f32_e64 v130, |v228|, |v229|
	v_max3_f32 v250, |v230|, |v231|, v130
	ds_read_b128 v[130:133], v251 offset:21504
	ds_read_b128 v[242:245], v251 offset:22528
	ds_read_b128 v[246:249], v251 offset:23552
	s_waitcnt lgkmcnt(1)
	v_pk_add_f32 v[202:203], v[244:245], 1.0 op_sel_hi:[1,0]
	v_pk_add_f32 v[204:205], v[242:243], 1.0 op_sel_hi:[1,0]
	v_pk_mul_f32 v[132:133], v[132:133], v[202:203]
	v_pk_mul_f32 v[202:203], v[130:131], v[204:205]
	s_waitcnt lgkmcnt(0)
	v_pk_fma_f32 v[130:131], v[132:133], v[200:201], v[248:249]
	v_pk_fma_f32 v[132:133], v[202:203], v[198:199], v[246:247]
	v_max_f32_e64 v198, |v130|, |v131|
	v_max3_f32 v198, |v132|, |v133|, v198
	v_max3_f32 v193, v193, v250, v198
	s_waitcnt lgkmcnt(0)
	s_nop 1
	v_max_f32_dpp v193, v193, v193 quad_perm:[1,0,3,2] row_mask:0xf bank_mask:0xf
	s_nop 1
	v_max_f32_dpp v193, v193, v193 quad_perm:[2,3,0,1] row_mask:0xf bank_mask:0xf
	s_nop 1
	v_max_f32_dpp v193, v193, v193 row_half_mirror row_mask:0xf bank_mask:0xf
	s_nop 1
	v_max_f32_dpp v193, v193, v193 row_mirror row_mask:0xf bank_mask:0xf
	v_mov_b32_e32 v198, v193
	s_nop 1
	v_permlane16_swap_b32 v193, v198
	v_max_f32_e32 v193, v193, v198
	v_mov_b32_e32 v198, v193
	s_nop 1
	v_permlane32_swap_b32 v193, v198
	v_max_f32_e32 v193, v193, v198
	v_cmp_neq_f32_e32 vcc, 0, v193
	s_nop 1
	v_cndmask_b32_e32 v193, 1.0, v193, vcc
	s_and_saveexec_b64 s[8:9], s[4:5]
	s_cbranch_execz .LBB0_1871
	s_lshl_b64 s[10:11], s[6:7], 2
	s_add_u32 s10, s34, s10
	s_addc_u32 s11, s35, s11
	v_mul_f32_e32 v198, 0x3c010204, v193
	global_store_dword v165, v198, s[10:11]

; __global__ void __launch_bounds__(NWAVES * 64, 2) fwd_kernel(Args a_unused) {
;     ...
; #pragma unroll
;         for (int q = 0; q < 4; ++q) sl[q] = rt_s[gw * 4 + q];
;         P12_LOAD(v, gw); P12_SUM();
.LBB0_2549:
	s_cmpk_gt_i32 s58, 0x3fff
	s_cbranch_scc1 .LBB0_2558
	s_waitcnt vmcnt(41)
	v_lshlrev_b32_e32 v92, 16, v72
	v_and_b32_e32 v93, 0xffff0000, v72
	v_lshlrev_b32_e32 v112, 16, v73
	v_and_b32_e32 v113, 0xffff0000, v73
	s_waitcnt vmcnt(40)
	v_lshlrev_b32_e32 v90, 16, v70
	v_and_b32_e32 v91, 0xffff0000, v70
	v_lshlrev_b32_e32 v110, 16, v71
	v_and_b32_e32 v111, 0xffff0000, v71
	s_waitcnt vmcnt(39)
	v_cvt_f32_i32_sdwa v71, sext(v38) dst_sel:DWORD dst_unused:UNUSED_PAD src0_sel:BYTE_3
	v_cvt_f32_i32_sdwa v70, sext(v38) dst_sel:DWORD dst_unused:UNUSED_PAD src0_sel:BYTE_2
	v_cvt_f32_i32_sdwa v73, sext(v38) dst_sel:DWORD dst_unused:UNUSED_PAD src0_sel:BYTE_1
	v_cvt_f32_i32_sdwa v72, sext(v38) dst_sel:DWORD dst_unused:UNUSED_PAD src0_sel:BYTE_0
	v_lshlrev_b32_e32 v96, 16, v76
	v_and_b32_e32 v97, 0xffff0000, v76
	v_lshlrev_b32_e32 v116, 16, v77
	v_and_b32_e32 v117, 0xffff0000, v77
	v_lshlrev_b32_e32 v94, 16, v74
	v_and_b32_e32 v95, 0xffff0000, v74
	v_lshlrev_b32_e32 v114, 16, v75
	v_and_b32_e32 v115, 0xffff0000, v75
	s_waitcnt vmcnt(29)
	v_cvt_f32_i32_sdwa v75, sext(v39) dst_sel:DWORD dst_unused:UNUSED_PAD src0_sel:BYTE_3
	v_cvt_f32_i32_sdwa v77, sext(v39) dst_sel:DWORD dst_unused:UNUSED_PAD src0_sel:BYTE_1
	v_cvt_f32_i32_sdwa v74, sext(v39) dst_sel:DWORD dst_unused:UNUSED_PAD src0_sel:BYTE_2
	v_cvt_f32_i32_sdwa v76, sext(v39) dst_sel:DWORD dst_unused:UNUSED_PAD src0_sel:BYTE_0
	v_pk_fma_f32 v[72:73], v[4:5], v[72:73], 0 op_sel_hi:[0,1,0]
	v_pk_fma_f32 v[70:71], v[4:5], v[70:71], 0 op_sel_hi:[0,1,0]
	s_waitcnt vmcnt(20)
	v_pk_fma_f32 v[70:71], v[20:21], v[74:75], v[70:71] op_sel_hi:[0,1,1]
	v_pk_fma_f32 v[72:73], v[20:21], v[76:77], v[72:73] op_sel_hi:[0,1,1]
	s_waitcnt vmcnt(19)
	v_cvt_f32_i32_sdwa v75, sext(v54) dst_sel:DWORD dst_unused:UNUSED_PAD src0_sel:BYTE_3
	v_cvt_f32_i32_sdwa v74, sext(v54) dst_sel:DWORD dst_unused:UNUSED_PAD src0_sel:BYTE_2
	v_cvt_f32_i32_sdwa v77, sext(v54) dst_sel:DWORD dst_unused:UNUSED_PAD src0_sel:BYTE_1
	v_cvt_f32_i32_sdwa v76, sext(v54) dst_sel:DWORD dst_unused:UNUSED_PAD src0_sel:BYTE_0
	v_lshlrev_b32_e32 v100, 16, v80
	v_and_b32_e32 v101, 0xffff0000, v80
	v_lshlrev_b32_e32 v120, 16, v81
	v_and_b32_e32 v121, 0xffff0000, v81
	v_lshlrev_b32_e32 v98, 16, v78
	v_and_b32_e32 v99, 0xffff0000, v78
	v_lshlrev_b32_e32 v118, 16, v79
	v_and_b32_e32 v119, 0xffff0000, v79
	s_waitcnt vmcnt(7)
	v_cvt_f32_i32_sdwa v79, sext(v55) dst_sel:DWORD dst_unused:UNUSED_PAD src0_sel:BYTE_3
	v_cvt_f32_i32_sdwa v81, sext(v55) dst_sel:DWORD dst_unused:UNUSED_PAD src0_sel:BYTE_1
	v_cvt_f32_i32_sdwa v78, sext(v55) dst_sel:DWORD dst_unused:UNUSED_PAD src0_sel:BYTE_2
	v_cvt_f32_i32_sdwa v80, sext(v55) dst_sel:DWORD dst_unused:UNUSED_PAD src0_sel:BYTE_0
	v_pk_fma_f32 v[72:73], v[16:17], v[76:77], v[72:73] op_sel_hi:[0,1,1]
	v_pk_fma_f32 v[70:71], v[16:17], v[74:75], v[70:71] op_sel_hi:[0,1,1]
	v_cvt_f32_i32_sdwa v75, sext(v40) dst_sel:DWORD dst_unused:UNUSED_PAD src0_sel:BYTE_3
	v_cvt_f32_i32_sdwa v74, sext(v40) dst_sel:DWORD dst_unused:UNUSED_PAD src0_sel:BYTE_2
	v_cvt_f32_i32_sdwa v77, sext(v40) dst_sel:DWORD dst_unused:UNUSED_PAD src0_sel:BYTE_1
	v_cvt_f32_i32_sdwa v76, sext(v40) dst_sel:DWORD dst_unused:UNUSED_PAD src0_sel:BYTE_0
	v_pk_fma_f32 v[70:71], v[24:25], v[78:79], v[70:71] op_sel_hi:[0,1,1]
	v_pk_fma_f32 v[72:73], v[24:25], v[80:81], v[72:73] op_sel_hi:[0,1,1]
	v_cvt_f32_i32_sdwa v79, sext(v41) dst_sel:DWORD dst_unused:UNUSED_PAD src0_sel:BYTE_3
	v_cvt_f32_i32_sdwa v81, sext(v41) dst_sel:DWORD dst_unused:UNUSED_PAD src0_sel:BYTE_1
	v_cvt_f32_i32_sdwa v78, sext(v41) dst_sel:DWORD dst_unused:UNUSED_PAD src0_sel:BYTE_2
	v_cvt_f32_i32_sdwa v80, sext(v41) dst_sel:DWORD dst_unused:UNUSED_PAD src0_sel:BYTE_0
	v_pk_fma_f32 v[76:77], v[4:5], v[76:77], 0 op_sel:[1,0,0] op_sel_hi:[1,1,0]
	v_pk_fma_f32 v[74:75], v[4:5], v[74:75], 0 op_sel:[1,0,0] op_sel_hi:[1,1,0]
	v_lshlrev_b32_e32 v104, 16, v84
	v_pk_fma_f32 v[74:75], v[20:21], v[78:79], v[74:75] op_sel:[1,0,0]
	v_pk_fma_f32 v[76:77], v[20:21], v[80:81], v[76:77] op_sel:[1,0,0]
	v_cvt_f32_i32_sdwa v79, sext(v56) dst_sel:DWORD dst_unused:UNUSED_PAD src0_sel:BYTE_3
	v_cvt_f32_i32_sdwa v78, sext(v56) dst_sel:DWORD dst_unused:UNUSED_PAD src0_sel:BYTE_2
	v_cvt_f32_i32_sdwa v81, sext(v56) dst_sel:DWORD dst_unused:UNUSED_PAD src0_sel:BYTE_1
	v_cvt_f32_i32_sdwa v80, sext(v56) dst_sel:DWORD dst_unused:UNUSED_PAD src0_sel:BYTE_0
	v_and_b32_e32 v105, 0xffff0000, v84
	v_lshlrev_b32_e32 v124, 16, v85
	v_and_b32_e32 v125, 0xffff0000, v85
	v_lshlrev_b32_e32 v102, 16, v82
	v_and_b32_e32 v103, 0xffff0000, v82
	v_lshlrev_b32_e32 v122, 16, v83
	v_and_b32_e32 v123, 0xffff0000, v83
	s_waitcnt vmcnt(6)
	v_cvt_f32_i32_sdwa v83, sext(v57) dst_sel:DWORD dst_unused:UNUSED_PAD src0_sel:BYTE_3
	v_cvt_f32_i32_sdwa v85, sext(v57) dst_sel:DWORD dst_unused:UNUSED_PAD src0_sel:BYTE_1
	v_cvt_f32_i32_sdwa v82, sext(v57) dst_sel:DWORD dst_unused:UNUSED_PAD src0_sel:BYTE_2
	v_cvt_f32_i32_sdwa v84, sext(v57) dst_sel:DWORD dst_unused:UNUSED_PAD src0_sel:BYTE_0
	v_pk_fma_f32 v[76:77], v[16:17], v[80:81], v[76:77] op_sel:[1,0,0]
	v_pk_fma_f32 v[74:75], v[16:17], v[78:79], v[74:75] op_sel:[1,0,0]
	v_cvt_f32_i32_sdwa v79, sext(v42) dst_sel:DWORD dst_unused:UNUSED_PAD src0_sel:BYTE_3
	v_cvt_f32_i32_sdwa v78, sext(v42) dst_sel:DWORD dst_unused:UNUSED_PAD src0_sel:BYTE_2
	v_cvt_f32_i32_sdwa v81, sext(v42) dst_sel:DWORD dst_unused:UNUSED_PAD src0_sel:BYTE_1
	v_cvt_f32_i32_sdwa v80, sext(v42) dst_sel:DWORD dst_unused:UNUSED_PAD src0_sel:BYTE_0
	v_pk_fma_f32 v[74:75], v[24:25], v[82:83], v[74:75] op_sel:[1,0,0]
	v_pk_fma_f32 v[76:77], v[24:25], v[84:85], v[76:77] op_sel:[1,0,0]
	v_cvt_f32_i32_sdwa v83, sext(v43) dst_sel:DWORD dst_unused:UNUSED_PAD src0_sel:BYTE_3
	v_cvt_f32_i32_sdwa v85, sext(v43) dst_sel:DWORD dst_unused:UNUSED_PAD src0_sel:BYTE_1
	v_cvt_f32_i32_sdwa v82, sext(v43) dst_sel:DWORD dst_unused:UNUSED_PAD src0_sel:BYTE_2
	v_cvt_f32_i32_sdwa v84, sext(v43) dst_sel:DWORD dst_unused:UNUSED_PAD src0_sel:BYTE_0
	v_pk_fma_f32 v[80:81], v[6:7], v[80:81], 0 op_sel_hi:[0,1,0]
	v_pk_fma_f32 v[78:79], v[6:7], v[78:79], 0 op_sel_hi:[0,1,0]
	v_pk_fma_f32 v[78:79], v[22:23], v[82:83], v[78:79] op_sel_hi:[0,1,1]
	v_pk_fma_f32 v[80:81], v[22:23], v[84:85], v[80:81] op_sel_hi:[0,1,1]
	v_cvt_f32_i32_sdwa v83, sext(v58) dst_sel:DWORD dst_unused:UNUSED_PAD src0_sel:BYTE_3
	v_cvt_f32_i32_sdwa v82, sext(v58) dst_sel:DWORD dst_unused:UNUSED_PAD src0_sel:BYTE_2
	v_cvt_f32_i32_sdwa v85, sext(v58) dst_sel:DWORD dst_unused:UNUSED_PAD src0_sel:BYTE_1
	v_cvt_f32_i32_sdwa v84, sext(v58) dst_sel:DWORD dst_unused:UNUSED_PAD src0_sel:BYTE_0
	s_waitcnt vmcnt(5)
; __global__ void __launch_bounds__(NWAVES * 64, 2) fwd_kernel(Args a_unused) {
;     ...
; #pragma unroll
;         for (int q = 0; q < 4; ++q) sl[q] = rt_s[gw * 4 + q];
;         P12_LOAD(v, gw); P12_SUM();
	v_cvt_f32_i32_sdwa v89, sext(v59) dst_sel:DWORD dst_unused:UNUSED_PAD src0_sel:BYTE_1
	v_cvt_f32_i32_sdwa v88, sext(v59) dst_sel:DWORD dst_unused:UNUSED_PAD src0_sel:BYTE_0
	v_cvt_f32_i32_sdwa v87, sext(v59) dst_sel:DWORD dst_unused:UNUSED_PAD src0_sel:BYTE_3
	v_cvt_f32_i32_sdwa v86, sext(v59) dst_sel:DWORD dst_unused:UNUSED_PAD src0_sel:BYTE_2
	v_pk_fma_f32 v[80:81], v[18:19], v[84:85], v[80:81] op_sel_hi:[0,1,1]
	v_pk_fma_f32 v[78:79], v[18:19], v[82:83], v[78:79] op_sel_hi:[0,1,1]
	v_cvt_f32_i32_sdwa v83, sext(v44) dst_sel:DWORD dst_unused:UNUSED_PAD src0_sel:BYTE_1
	v_cvt_f32_i32_sdwa v82, sext(v44) dst_sel:DWORD dst_unused:UNUSED_PAD src0_sel:BYTE_0
	v_cvt_f32_i32_sdwa v85, sext(v44) dst_sel:DWORD dst_unused:UNUSED_PAD src0_sel:BYTE_3
	v_cvt_f32_i32_sdwa v84, sext(v44) dst_sel:DWORD dst_unused:UNUSED_PAD src0_sel:BYTE_2
	v_pk_fma_f32 v[80:81], v[26:27], v[88:89], v[80:81] op_sel_hi:[0,1,1]
	v_cvt_f32_i32_sdwa v89, sext(v45) dst_sel:DWORD dst_unused:UNUSED_PAD src0_sel:BYTE_3
	v_cvt_f32_i32_sdwa v107, sext(v45) dst_sel:DWORD dst_unused:UNUSED_PAD src0_sel:BYTE_1
	v_cvt_f32_i32_sdwa v88, sext(v45) dst_sel:DWORD dst_unused:UNUSED_PAD src0_sel:BYTE_2
	v_cvt_f32_i32_sdwa v106, sext(v45) dst_sel:DWORD dst_unused:UNUSED_PAD src0_sel:BYTE_0
	v_pk_fma_f32 v[78:79], v[26:27], v[86:87], v[78:79] op_sel_hi:[0,1,1]
	v_mov_b32_e32 v86, v7
	v_pk_fma_f32 v[82:83], v[86:87], v[82:83], 0 op_sel_hi:[0,1,0]
	v_pk_fma_f32 v[84:85], v[86:87], v[84:85], 0 op_sel_hi:[0,1,0]
	v_mov_b32_e32 v86, v23
	v_pk_fma_f32 v[84:85], v[86:87], v[88:89], v[84:85] op_sel_hi:[0,1,1]
	v_pk_fma_f32 v[82:83], v[86:87], v[106:107], v[82:83] op_sel_hi:[0,1,1]
	v_cvt_f32_i32_sdwa v87, sext(v60) dst_sel:DWORD dst_unused:UNUSED_PAD src0_sel:BYTE_1
	v_cvt_f32_i32_sdwa v86, sext(v60) dst_sel:DWORD dst_unused:UNUSED_PAD src0_sel:BYTE_0
	v_cvt_f32_i32_sdwa v89, sext(v60) dst_sel:DWORD dst_unused:UNUSED_PAD src0_sel:BYTE_3
	v_cvt_f32_i32_sdwa v88, sext(v60) dst_sel:DWORD dst_unused:UNUSED_PAD src0_sel:BYTE_2
	v_mov_b32_e32 v106, v19
	v_pk_fma_f32 v[82:83], v[106:107], v[86:87], v[82:83] op_sel_hi:[0,1,1]
	s_waitcnt vmcnt(4)
	v_cvt_f32_i32_sdwa v87, sext(v61) dst_sel:DWORD dst_unused:UNUSED_PAD src0_sel:BYTE_3
	v_cvt_f32_i32_sdwa v109, sext(v61) dst_sel:DWORD dst_unused:UNUSED_PAD src0_sel:BYTE_1
	v_cvt_f32_i32_sdwa v86, sext(v61) dst_sel:DWORD dst_unused:UNUSED_PAD src0_sel:BYTE_2
	v_cvt_f32_i32_sdwa v108, sext(v61) dst_sel:DWORD dst_unused:UNUSED_PAD src0_sel:BYTE_0
	v_pk_fma_f32 v[84:85], v[106:107], v[88:89], v[84:85] op_sel_hi:[0,1,1]
	v_mov_b32_e32 v88, v27
	v_pk_fma_f32 v[86:87], v[88:89], v[86:87], v[84:85] op_sel_hi:[0,1,1]
	v_pk_fma_f32 v[88:89], v[88:89], v[108:109], v[82:83] op_sel_hi:[0,1,1]
	v_cvt_f32_i32_sdwa v83, sext(v46) dst_sel:DWORD dst_unused:UNUSED_PAD src0_sel:BYTE_3
	v_cvt_f32_i32_sdwa v82, sext(v46) dst_sel:DWORD dst_unused:UNUSED_PAD src0_sel:BYTE_2
	v_cvt_f32_i32_sdwa v85, sext(v46) dst_sel:DWORD dst_unused:UNUSED_PAD src0_sel:BYTE_1
	v_cvt_f32_i32_sdwa v84, sext(v46) dst_sel:DWORD dst_unused:UNUSED_PAD src0_sel:BYTE_0
	v_cvt_f32_i32_sdwa v107, sext(v47) dst_sel:DWORD dst_unused:UNUSED_PAD src0_sel:BYTE_3
	v_cvt_f32_i32_sdwa v109, sext(v47) dst_sel:DWORD dst_unused:UNUSED_PAD src0_sel:BYTE_1
	v_cvt_f32_i32_sdwa v106, sext(v47) dst_sel:DWORD dst_unused:UNUSED_PAD src0_sel:BYTE_2
	v_cvt_f32_i32_sdwa v108, sext(v47) dst_sel:DWORD dst_unused:UNUSED_PAD src0_sel:BYTE_0
	v_pk_fma_f32 v[84:85], v[0:1], v[84:85], 0 op_sel_hi:[0,1,0]
	v_pk_fma_f32 v[82:83], v[0:1], v[82:83], 0 op_sel_hi:[0,1,0]
	v_pk_fma_f32 v[82:83], v[28:29], v[106:107], v[82:83] op_sel_hi:[0,1,1]
	v_pk_fma_f32 v[84:85], v[28:29], v[108:109], v[84:85] op_sel_hi:[0,1,1]
	v_cvt_f32_i32_sdwa v107, sext(v62) dst_sel:DWORD dst_unused:UNUSED_PAD src0_sel:BYTE_3
	v_cvt_f32_i32_sdwa v106, sext(v62) dst_sel:DWORD dst_unused:UNUSED_PAD src0_sel:BYTE_2
	v_cvt_f32_i32_sdwa v109, sext(v62) dst_sel:DWORD dst_unused:UNUSED_PAD src0_sel:BYTE_1
	v_cvt_f32_i32_sdwa v108, sext(v62) dst_sel:DWORD dst_unused:UNUSED_PAD src0_sel:BYTE_0
	s_waitcnt vmcnt(3)
	v_cvt_f32_i32_sdwa v127, sext(v63) dst_sel:DWORD dst_unused:UNUSED_PAD src0_sel:BYTE_3
	v_cvt_f32_i32_sdwa v129, sext(v63) dst_sel:DWORD dst_unused:UNUSED_PAD src0_sel:BYTE_1
	v_cvt_f32_i32_sdwa v126, sext(v63) dst_sel:DWORD dst_unused:UNUSED_PAD src0_sel:BYTE_2
	v_cvt_f32_i32_sdwa v128, sext(v63) dst_sel:DWORD dst_unused:UNUSED_PAD src0_sel:BYTE_0
	v_pk_fma_f32 v[84:85], v[12:13], v[108:109], v[84:85] op_sel_hi:[0,1,1]
	v_pk_fma_f32 v[82:83], v[12:13], v[106:107], v[82:83] op_sel_hi:[0,1,1]
	v_pk_fma_f32 v[140:141], v[32:33], v[126:127], v[82:83] op_sel_hi:[0,1,1]
	v_pk_fma_f32 v[142:143], v[32:33], v[128:129], v[84:85] op_sel_hi:[0,1,1]
	v_cvt_f32_i32_sdwa v83, sext(v48) dst_sel:DWORD dst_unused:UNUSED_PAD src0_sel:BYTE_1
	v_cvt_f32_i32_sdwa v82, sext(v48) dst_sel:DWORD dst_unused:UNUSED_PAD src0_sel:BYTE_0
	v_cvt_f32_i32_sdwa v85, sext(v48) dst_sel:DWORD dst_unused:UNUSED_PAD src0_sel:BYTE_3
	v_cvt_f32_i32_sdwa v84, sext(v48) dst_sel:DWORD dst_unused:UNUSED_PAD src0_sel:BYTE_2
	v_cvt_f32_i32_sdwa v109, sext(v49) dst_sel:DWORD dst_unused:UNUSED_PAD src0_sel:BYTE_3
	v_cvt_f32_i32_sdwa v127, sext(v49) dst_sel:DWORD dst_unused:UNUSED_PAD src0_sel:BYTE_1
	v_cvt_f32_i32_sdwa v108, sext(v49) dst_sel:DWORD dst_unused:UNUSED_PAD src0_sel:BYTE_2
	v_cvt_f32_i32_sdwa v126, sext(v49) dst_sel:DWORD dst_unused:UNUSED_PAD src0_sel:BYTE_0
	v_mov_b32_e32 v106, v1
	v_pk_fma_f32 v[82:83], v[106:107], v[82:83], 0 op_sel_hi:[0,1,0]
	v_pk_fma_f32 v[84:85], v[106:107], v[84:85], 0 op_sel_hi:[0,1,0]
	v_mov_b32_e32 v106, v29
	v_pk_fma_f32 v[84:85], v[106:107], v[108:109], v[84:85] op_sel_hi:[0,1,1]
	v_pk_fma_f32 v[82:83], v[106:107], v[126:127], v[82:83] op_sel_hi:[0,1,1]
	v_cvt_f32_i32_sdwa v107, sext(v64) dst_sel:DWORD dst_unused:UNUSED_PAD src0_sel:BYTE_1
	v_cvt_f32_i32_sdwa v106, sext(v64) dst_sel:DWORD dst_unused:UNUSED_PAD src0_sel:BYTE_0
	v_cvt_f32_i32_sdwa v109, sext(v64) dst_sel:DWORD dst_unused:UNUSED_PAD src0_sel:BYTE_3
	v_cvt_f32_i32_sdwa v108, sext(v64) dst_sel:DWORD dst_unused:UNUSED_PAD src0_sel:BYTE_2
	v_mov_b32_e32 v126, v13
	v_pk_fma_f32 v[82:83], v[126:127], v[106:107], v[82:83] op_sel_hi:[0,1,1]
	s_waitcnt vmcnt(2)
; __global__ void __launch_bounds__(NWAVES * 64, 2) fwd_kernel(Args a_unused) {
;     ...
; #pragma unroll
;         for (int q = 0; q < 4; ++q) sl[q] = rt_s[gw * 4 + q];
;         P12_LOAD(v, gw); P12_SUM();
	v_cvt_f32_i32_sdwa v107, sext(v65) dst_sel:DWORD dst_unused:UNUSED_PAD src0_sel:BYTE_3
	v_cvt_f32_i32_sdwa v129, sext(v65) dst_sel:DWORD dst_unused:UNUSED_PAD src0_sel:BYTE_1
	v_cvt_f32_i32_sdwa v106, sext(v65) dst_sel:DWORD dst_unused:UNUSED_PAD src0_sel:BYTE_2
	v_cvt_f32_i32_sdwa v128, sext(v65) dst_sel:DWORD dst_unused:UNUSED_PAD src0_sel:BYTE_0
	v_pk_fma_f32 v[84:85], v[126:127], v[108:109], v[84:85] op_sel_hi:[0,1,1]
	v_mov_b32_e32 v108, v33
	v_pk_fma_f32 v[152:153], v[108:109], v[106:107], v[84:85] op_sel_hi:[0,1,1]
	v_pk_fma_f32 v[154:155], v[108:109], v[128:129], v[82:83] op_sel_hi:[0,1,1]
	v_cvt_f32_i32_sdwa v83, sext(v50) dst_sel:DWORD dst_unused:UNUSED_PAD src0_sel:BYTE_3
	v_cvt_f32_i32_sdwa v82, sext(v50) dst_sel:DWORD dst_unused:UNUSED_PAD src0_sel:BYTE_2
	v_cvt_f32_i32_sdwa v85, sext(v50) dst_sel:DWORD dst_unused:UNUSED_PAD src0_sel:BYTE_1
	v_cvt_f32_i32_sdwa v84, sext(v50) dst_sel:DWORD dst_unused:UNUSED_PAD src0_sel:BYTE_0
	v_cvt_f32_i32_sdwa v107, sext(v51) dst_sel:DWORD dst_unused:UNUSED_PAD src0_sel:BYTE_3
	v_cvt_f32_i32_sdwa v109, sext(v51) dst_sel:DWORD dst_unused:UNUSED_PAD src0_sel:BYTE_1
	v_cvt_f32_i32_sdwa v106, sext(v51) dst_sel:DWORD dst_unused:UNUSED_PAD src0_sel:BYTE_2
	v_cvt_f32_i32_sdwa v108, sext(v51) dst_sel:DWORD dst_unused:UNUSED_PAD src0_sel:BYTE_0
	v_pk_fma_f32 v[84:85], v[2:3], v[84:85], 0 op_sel_hi:[0,1,0]
	v_pk_fma_f32 v[82:83], v[2:3], v[82:83], 0 op_sel_hi:[0,1,0]
	v_pk_fma_f32 v[82:83], v[30:31], v[106:107], v[82:83] op_sel_hi:[0,1,1]
	v_pk_fma_f32 v[84:85], v[30:31], v[108:109], v[84:85] op_sel_hi:[0,1,1]
	v_cvt_f32_i32_sdwa v107, sext(v66) dst_sel:DWORD dst_unused:UNUSED_PAD src0_sel:BYTE_3
	v_cvt_f32_i32_sdwa v106, sext(v66) dst_sel:DWORD dst_unused:UNUSED_PAD src0_sel:BYTE_2
	v_cvt_f32_i32_sdwa v109, sext(v66) dst_sel:DWORD dst_unused:UNUSED_PAD src0_sel:BYTE_1
	v_cvt_f32_i32_sdwa v108, sext(v66) dst_sel:DWORD dst_unused:UNUSED_PAD src0_sel:BYTE_0
	s_waitcnt vmcnt(1)
	v_cvt_f32_i32_sdwa v127, sext(v67) dst_sel:DWORD dst_unused:UNUSED_PAD src0_sel:BYTE_3
	v_cvt_f32_i32_sdwa v129, sext(v67) dst_sel:DWORD dst_unused:UNUSED_PAD src0_sel:BYTE_1
	v_cvt_f32_i32_sdwa v126, sext(v67) dst_sel:DWORD dst_unused:UNUSED_PAD src0_sel:BYTE_2
	v_cvt_f32_i32_sdwa v128, sext(v67) dst_sel:DWORD dst_unused:UNUSED_PAD src0_sel:BYTE_0
	v_pk_fma_f32 v[84:85], v[14:15], v[108:109], v[84:85] op_sel_hi:[0,1,1]
	v_pk_fma_f32 v[82:83], v[14:15], v[106:107], v[82:83] op_sel_hi:[0,1,1]
	v_pk_fma_f32 v[160:161], v[34:35], v[126:127], v[82:83] op_sel_hi:[0,1,1]
	v_pk_fma_f32 v[166:167], v[34:35], v[128:129], v[84:85] op_sel_hi:[0,1,1]
	v_cvt_f32_i32_sdwa v83, sext(v52) dst_sel:DWORD dst_unused:UNUSED_PAD src0_sel:BYTE_1
	v_cvt_f32_i32_sdwa v82, sext(v52) dst_sel:DWORD dst_unused:UNUSED_PAD src0_sel:BYTE_0
	v_cvt_f32_i32_sdwa v85, sext(v52) dst_sel:DWORD dst_unused:UNUSED_PAD src0_sel:BYTE_3
	v_cvt_f32_i32_sdwa v84, sext(v52) dst_sel:DWORD dst_unused:UNUSED_PAD src0_sel:BYTE_2
	v_cvt_f32_i32_sdwa v109, sext(v53) dst_sel:DWORD dst_unused:UNUSED_PAD src0_sel:BYTE_3
	v_cvt_f32_i32_sdwa v127, sext(v53) dst_sel:DWORD dst_unused:UNUSED_PAD src0_sel:BYTE_1
	v_cvt_f32_i32_sdwa v108, sext(v53) dst_sel:DWORD dst_unused:UNUSED_PAD src0_sel:BYTE_2
	v_cvt_f32_i32_sdwa v126, sext(v53) dst_sel:DWORD dst_unused:UNUSED_PAD src0_sel:BYTE_0
	v_mov_b32_e32 v106, v3
	v_pk_fma_f32 v[82:83], v[106:107], v[82:83], 0 op_sel_hi:[0,1,0]
	v_pk_fma_f32 v[84:85], v[106:107], v[84:85], 0 op_sel_hi:[0,1,0]
	v_mov_b32_e32 v106, v31
	v_pk_fma_f32 v[84:85], v[106:107], v[108:109], v[84:85] op_sel_hi:[0,1,1]
	v_pk_fma_f32 v[82:83], v[106:107], v[126:127], v[82:83] op_sel_hi:[0,1,1]
	v_cvt_f32_i32_sdwa v107, sext(v68) dst_sel:DWORD dst_unused:UNUSED_PAD src0_sel:BYTE_1
	v_cvt_f32_i32_sdwa v106, sext(v68) dst_sel:DWORD dst_unused:UNUSED_PAD src0_sel:BYTE_0
	v_cvt_f32_i32_sdwa v109, sext(v68) dst_sel:DWORD dst_unused:UNUSED_PAD src0_sel:BYTE_3
	v_cvt_f32_i32_sdwa v108, sext(v68) dst_sel:DWORD dst_unused:UNUSED_PAD src0_sel:BYTE_2
	v_mov_b32_e32 v126, v15
	v_pk_fma_f32 v[82:83], v[126:127], v[106:107], v[82:83] op_sel_hi:[0,1,1]
	s_waitcnt vmcnt(0)
; __global__ void __launch_bounds__(NWAVES * 64, 2) fwd_kernel(Args a_unused) {
;     ...
; #pragma unroll
;         for (int q = 0; q < 4; ++q) sl[q] = rt_s[gw * 4 + q];
;         P12_LOAD(v, gw); P12_SUM();
;         if (gw + NGW < NTOK) {
; #pragma unroll
;             for (int q = 0; q < 4; ++q) sl[q] = rt_s[(gw + NGW) * 4 + q];
;         }
;         for (int m = gw; m < NTOK; m += NGW) {
;             const bool more = m + NGW < NTOK;
;             if (more) { P12_LOAD(vn, m + NGW);
;                 if (m + 2 * NGW < NTOK) {
; #pragma unroll
;                     for (int q = 0; q < 4; ++q) sl[q] = rt_s[(m + 2 * NGW) * 4 + q]; } }
;             float ss = 0.f;
; #pragma unroll
;             for (int j = 0; j < 8; ++j) { const f32x4 m5 = *(const f32x4*)(modl + 5 * 2048 + 4 * lane + 256 * j); v[j] = v[j] + m5 * y[j]; ss += v[j][0] * v[j][0] + v[j][1] * v[j][1] + v[j][2] * v[j][2] + v[j][3] * v[j][3]; }
;             const float rstd = rsqrtf(wave_sum(ss) * (1.0f / D) + EPS);
;             float* orow = A->out + (size_t)m * D + 4 * lane;
; #pragma unroll
;             for (int j = 0; j < 8; ++j) { const f32x4 fg = *(const f32x4*)(A->final_g + 4 * lane + 256 * j); *(f32x4*)(orow + 256 * j) = v[j] * rstd * fg; }
	v_cvt_f32_i32_sdwa v107, sext(v69) dst_sel:DWORD dst_unused:UNUSED_PAD src0_sel:BYTE_3
	v_cvt_f32_i32_sdwa v106, sext(v69) dst_sel:DWORD dst_unused:UNUSED_PAD src0_sel:BYTE_2
	v_cvt_f32_i32_sdwa v129, sext(v69) dst_sel:DWORD dst_unused:UNUSED_PAD src0_sel:BYTE_1
	v_cvt_f32_i32_sdwa v128, sext(v69) dst_sel:DWORD dst_unused:UNUSED_PAD src0_sel:BYTE_0
	v_pk_fma_f32 v[84:85], v[126:127], v[108:109], v[84:85] op_sel_hi:[0,1,1]
	v_mov_b32_e32 v108, v35
	v_pk_fma_f32 v[168:169], v[108:109], v[106:107], v[84:85] op_sel_hi:[0,1,1]
	v_mbcnt_lo_u32_b32 v106, -1, 0
	v_mbcnt_hi_u32_b32 v106, -1, v106
	v_and_b32_e32 v107, 64, v106
	v_pk_fma_f32 v[170:171], v[108:109], v[128:129], v[82:83] op_sel_hi:[0,1,1]
	v_add_u32_e32 v107, 64, v107
	v_xor_b32_e32 v108, 1, v106
	v_cmp_lt_i32_e32 vcc, v108, v107
	v_lshlrev_b32_e32 v82, 2, v164
	v_mov_b32_e32 v83, 0
	v_cndmask_b32_e32 v108, v106, v108, vcc
	v_lshlrev_b32_e32 v176, 2, v108
	v_xor_b32_e32 v108, 2, v106
	v_cmp_lt_i32_e32 vcc, v108, v107
	v_lshl_add_u64 v[130:131], s[8:9], 0, v[82:83]
	s_mov_b64 s[0:1], 0x10a000
	v_cndmask_b32_e32 v108, v106, v108, vcc
	v_lshlrev_b32_e32 v177, 2, v108
	v_xor_b32_e32 v108, 4, v106
	v_cmp_lt_i32_e32 vcc, v108, v107
	s_load_dwordx4 s[4:7], s[78:79], 0xb8
	v_lshl_add_u64 v[84:85], v[130:131], 0, s[0:1]
	v_cndmask_b32_e32 v108, v106, v108, vcc
	v_lshlrev_b32_e32 v178, 2, v108
	v_xor_b32_e32 v108, 8, v106
	v_cmp_lt_i32_e32 vcc, v108, v107
	s_mov_b64 s[0:1], 0x10b000
	s_lshl_b32 s16, s33, 4
	v_cndmask_b32_e32 v108, v106, v108, vcc
	v_lshlrev_b32_e32 v179, 2, v108
	v_xor_b32_e32 v108, 16, v106
	v_cmp_lt_i32_e32 vcc, v108, v107
	v_mov_b32_e32 v148, v15
	v_mov_b32_e32 v149, v35
	v_cndmask_b32_e32 v108, v106, v108, vcc
	v_lshlrev_b32_e32 v180, 2, v108
	v_xor_b32_e32 v108, 32, v106
	v_cmp_lt_i32_e32 vcc, v108, v107
	v_mov_b32_e32 v15, v34
	v_mov_b32_e32 v34, v13
	v_cndmask_b32_e32 v106, v106, v108, vcc
	v_lshl_add_u64 v[108:109], v[130:131], 0, s[0:1]
	s_mov_b64 s[0:1], 0x10b400
	v_lshl_add_u64 v[126:127], v[130:131], 0, s[0:1]
	s_mov_b64 s[0:1], 0x10b800
	v_lshl_add_u64 v[128:129], v[130:131], 0, s[0:1]
	s_mov_b64 s[0:1], 0x10bc00
	v_lshlrev_b32_e32 v181, 2, v106
	s_waitcnt lgkmcnt(0)
	v_lshl_add_u64 v[106:107], s[4:5], 0, v[82:83]
	v_lshl_add_u64 v[130:131], v[130:131], 0, s[0:1]
	s_mov_b64 s[0:1], 0x1000
	s_lshl_b64 s[4:5], s[58:59], 13
	v_lshl_add_u64 v[132:133], v[106:107], 0, s[0:1]
	s_mov_b64 s[0:1], 0x1400
	s_add_u32 s4, s6, s4
	v_lshl_add_u64 v[134:135], v[106:107], 0, s[0:1]
	s_mov_b64 s[0:1], 0x1800
	v_lshlrev_b32_e32 v82, 4, v162
	s_addc_u32 s5, s7, s5
	v_lshl_add_u64 v[136:137], v[106:107], 0, s[0:1]
	s_mov_b64 s[0:1], 0x1c00
	v_mov_b32_e32 v35, v33
	v_mov_b32_e32 v13, v32
	v_mov_b32_e32 v32, v19
	v_mov_b32_e32 v33, v27
	v_mov_b32_e32 v19, v26
	v_mov_b32_e32 v26, v5
	v_mov_b32_e32 v27, v21
	v_mov_b32_e32 v5, v20
	v_lshl_add_u64 v[20:21], s[4:5], 0, v[82:83]
	s_ashr_i32 s57, s56, 31
	s_ashr_i32 s11, s10, 31
	v_lshl_add_u64 v[138:139], v[106:107], 0, s[0:1]
	v_lshl_add_u64 v[144:145], v[20:21], 0, s[0:1]
	s_lshl_b64 s[4:5], s[56:57], 13
	s_lshl_b64 s[0:1], s[10:11], 12
	s_add_u32 s0, s8, s0
	v_mov_b32_e32 v147, v83
	s_addc_u32 s1, s9, s1
	v_lshl_add_u64 v[20:21], s[0:1], 0, v[146:147]
	s_mov_b64 s[0:1], 0x5fc00e00
	v_lshl_add_u64 v[146:147], v[20:21], 0, s[0:1]
	s_add_i32 s0, s96, s16
	s_add_i32 s0, s0, s95
	v_mov_b32_e32 v150, v3
	v_mov_b32_e32 v151, v31
	v_mov_b32_e32 v3, v30
	v_mov_b32_e32 v156, v1
	v_mov_b32_e32 v157, v29
	v_mov_b32_e32 v1, v28
	v_mov_b32_e32 v158, v7
	v_mov_b32_e32 v159, v23
	v_mov_b32_e32 v7, v22
	v_mov_b32_e32 v22, v17
	v_mov_b32_e32 v23, v25
	v_mov_b32_e32 v17, v24
	s_lshl_b64 s[6:7], s[56:57], 12
	s_lshl_b32 s8, s0, 2
	s_lshl_b32 s17, s33, 5
	v_mov_b32_e32 v82, 0x358637bd
	s_mov_b32 s18, 0x800000
	s_movk_i32 s19, 0xf000
	s_lshl_b32 s0, s96, 10
	v_mov_b32_e32 v238, s0
	v_mov_b32_e32 v239, 0
	v_lshl_add_u64 v[240:241], v[106:107], 0, v[238:239]
	global_load_dwordx4 v[242:245], v[240:241], off
	v_lshlrev_b32_e32 v246, 4, v162
	v_add_u32_e32 v247, s0, v246
	s_waitcnt vmcnt(0)
	ds_write_b128 v247, v[242:245]
	s_waitcnt lgkmcnt(0)
	s_barrier
	s_branch .LBB0_2552

; __global__ void __launch_bounds__(NWAVES * 64, 2) fwd_kernel(Args a_unused) {
;     ...
;             float ss = 0.f;
; #pragma unroll
;             for (int j = 0; j < 8; ++j) { const f32x4 m5 = *(const f32x4*)(modl + 5 * 2048 + 4 * lane + 256 * j); v[j] = v[j] + m5 * y[j]; ss += v[j][0] * v[j][0] + v[j][1] * v[j][1] + v[j][2] * v[j][2] + v[j][3] * v[j][3]; }
;             const float rstd = rsqrtf(wave_sum(ss) * (1.0f / D) + EPS);
;             float* orow = A->out + (size_t)m * D + 4 * lane;
; #pragma unroll
;             for (int j = 0; j < 8; ++j) { const f32x4 fg = *(const f32x4*)(A->final_g + 4 * lane + 256 * j); *(f32x4*)(orow + 256 * j) = v[j] * rstd * fg; }
.LBB0_2556:
	global_load_dwordx4 v[28:31], v[84:85], off
	global_load_dwordx4 v[206:209], v[84:85], off offset:1024
	global_load_dwordx4 v[210:213], v[84:85], off offset:2048
	global_load_dwordx4 v[214:217], v[84:85], off offset:3072
	global_load_dwordx4 v[218:221], v[108:109], off
	global_load_dwordx4 v[222:225], v[126:127], off
	global_load_dwordx4 v[226:229], v[128:129], off
	global_load_dwordx4 v[230:233], v[130:131], off
	global_load_dwordx4 v[234:237], v[106:107], off
	s_waitcnt vmcnt(8)
	v_pk_fma_f32 v[104:105], v[28:29], v[72:73], v[104:105]
	s_waitcnt vmcnt(7)
	v_pk_fma_f32 v[102:103], v[206:207], v[76:77], v[102:103]
	s_waitcnt vmcnt(6)
	v_pk_fma_f32 v[100:101], v[210:211], v[80:81], v[100:101]
	s_waitcnt vmcnt(5)
	v_pk_fma_f32 v[98:99], v[214:215], v[88:89], v[98:99]
	s_waitcnt vmcnt(4)
	v_pk_fma_f32 v[96:97], v[218:219], v[142:143], v[96:97]
	s_waitcnt vmcnt(3)
	v_pk_fma_f32 v[94:95], v[222:223], v[154:155], v[94:95]
	v_mul_f32_e32 v214, v105, v105
	v_mul_f32_e32 v215, v103, v103
	v_pk_fma_f32 v[124:125], v[30:31], v[70:71], v[124:125]
	v_pk_fma_f32 v[122:123], v[208:209], v[74:75], v[122:123]
	v_pk_fma_f32 v[118:119], v[216:217], v[86:87], v[118:119]
	v_mul_f32_e32 v216, v101, v101
	v_mov_b32_e32 v24, v97
	v_mov_b32_e32 v25, v95
	v_fmac_f32_e32 v214, v104, v104
	v_fmac_f32_e32 v215, v102, v102
	v_pk_fma_f32 v[120:121], v[212:213], v[78:79], v[120:121]
	v_pk_fma_f32 v[116:117], v[220:221], v[140:141], v[116:117]
	v_pk_fma_f32 v[114:115], v[224:225], v[152:153], v[114:115]
	v_mul_f32_e32 v217, v99, v99
	v_mov_b32_e32 v20, v96
	v_mov_b32_e32 v21, v94
	v_fmac_f32_e32 v216, v100, v100
	v_pk_mul_f32 v[24:25], v[24:25], v[24:25]
	v_fmac_f32_e32 v214, v124, v124
	v_fmac_f32_e32 v215, v122, v122
	s_waitcnt vmcnt(2)
	v_pk_fma_f32 v[92:93], v[226:227], v[166:167], v[92:93]
	s_waitcnt vmcnt(1)
	v_pk_fma_f32 v[90:91], v[230:231], v[170:171], v[90:91]
	v_mov_b32_e32 v28, v116
	v_mov_b32_e32 v29, v114
	v_fmac_f32_e32 v217, v98, v98
	v_fmac_f32_e32 v216, v120, v120
	v_pk_fma_f32 v[20:21], v[20:21], v[20:21], v[24:25]
	v_fmac_f32_e32 v214, v125, v125
	v_fmac_f32_e32 v215, v123, v123
	v_mov_b32_e32 v208, v93
	v_mov_b32_e32 v209, v91
	v_fmac_f32_e32 v217, v118, v118
	v_fmac_f32_e32 v216, v121, v121
	v_pk_fma_f32 v[20:21], v[28:29], v[28:29], v[20:21]
	v_add_f32_e32 v28, v214, v215
	v_pk_fma_f32 v[112:113], v[228:229], v[160:161], v[112:113]
	v_pk_fma_f32 v[110:111], v[232:233], v[168:169], v[110:111]
	v_mov_b32_e32 v30, v117
	v_mov_b32_e32 v31, v115
	v_mov_b32_e32 v206, v92
	v_mov_b32_e32 v207, v90
	v_pk_mul_f32 v[208:209], v[208:209], v[208:209]
	v_fmac_f32_e32 v217, v119, v119
	v_add_f32_e32 v28, v28, v216
	v_mov_b32_e32 v210, v112
	v_mov_b32_e32 v211, v110
	v_pk_fma_f32 v[24:25], v[206:207], v[206:207], v[208:209]
	v_pk_fma_f32 v[20:21], v[30:31], v[30:31], v[20:21]
	v_add_f32_e32 v28, v28, v217
	v_mov_b32_e32 v212, v113
	v_mov_b32_e32 v213, v111
	v_pk_fma_f32 v[24:25], v[210:211], v[210:211], v[24:25]
	v_add_f32_e32 v20, v28, v20
	v_pk_fma_f32 v[24:25], v[212:213], v[212:213], v[24:25]
	v_add_f32_e32 v20, v20, v21
	v_add_f32_e32 v20, v20, v24
	v_add_f32_e32 v20, v20, v25
	s_waitcnt lgkmcnt(0)
	s_nop 1
	v_add_f32_dpp v20, v20, v20 quad_perm:[1,0,3,2] row_mask:0xf bank_mask:0xf
	s_nop 1
	v_add_f32_dpp v20, v20, v20 quad_perm:[2,3,0,1] row_mask:0xf bank_mask:0xf
	s_nop 1
	v_add_f32_dpp v20, v20, v20 row_half_mirror row_mask:0xf bank_mask:0xf
	s_nop 1
	v_add_f32_dpp v20, v20, v20 row_mirror row_mask:0xf bank_mask:0xf
	v_mov_b32_e32 v21, v20
	s_nop 1
	v_permlane16_swap_b32 v20, v21
	v_add_f32_e32 v20, v20, v21
	v_mov_b32_e32 v21, v20
	s_nop 1
	v_permlane32_swap_b32 v20, v21
	v_add_f32_e32 v20, v20, v21
	v_fmamk_f32 v20, v20, 0x3a000000, v82
	v_mul_f32_e32 v21, 0x4b800000, v20
	v_cmp_gt_f32_e32 vcc, s18, v20
	s_nop 1
	v_cndmask_b32_e32 v20, v20, v21, vcc
	v_rsq_f32_e32 v24, v20
	v_add_co_u32_e64 v20, s[0:1], s19, v144
	v_mul_f32_e32 v25, 0x45800000, v24
	v_cndmask_b32_e32 v24, v24, v25, vcc
	v_pk_mul_f32 v[28:29], v[24:25], v[104:105] op_sel_hi:[0,1]
	v_pk_mul_f32 v[30:31], v[24:25], v[124:125] op_sel_hi:[0,1]
	v_addc_co_u32_e64 v21, s[0:1], -1, v145, s[0:1]
	s_waitcnt vmcnt(0)
	v_pk_mul_f32 v[30:31], v[236:237], v[30:31]
	v_pk_mul_f32 v[28:29], v[234:235], v[28:29]
	global_store_dwordx4 v[20:21], v[28:31], off offset:-3072
	s_nop 0
	ds_read_b128 v[28:31], v246 offset:1024
	v_pk_mul_f32 v[206:207], v[24:25], v[122:123] op_sel_hi:[0,1]
	v_pk_mul_f32 v[208:209], v[24:25], v[102:103] op_sel_hi:[0,1]
	s_andn2_b64 vcc, exec, s[12:13]
	s_waitcnt lgkmcnt(0)
	v_pk_mul_f32 v[28:29], v[28:29], v[208:209]
	v_pk_mul_f32 v[30:31], v[30:31], v[206:207]
	global_store_dwordx4 v[20:21], v[28:31], off offset:-2048
	s_nop 0
	ds_read_b128 v[28:31], v246 offset:2048
	v_pk_mul_f32 v[206:207], v[24:25], v[120:121] op_sel_hi:[0,1]
	v_pk_mul_f32 v[208:209], v[24:25], v[100:101] op_sel_hi:[0,1]
	s_waitcnt lgkmcnt(0)
	v_pk_mul_f32 v[28:29], v[28:29], v[208:209]
	v_pk_mul_f32 v[30:31], v[30:31], v[206:207]
	global_store_dwordx4 v[20:21], v[28:31], off offset:-1024
	s_nop 0
	ds_read_b128 v[28:31], v246 offset:3072
	v_pk_mul_f32 v[20:21], v[24:25], v[118:119] op_sel_hi:[0,1]
	v_pk_mul_f32 v[206:207], v[24:25], v[98:99] op_sel_hi:[0,1]
	s_waitcnt lgkmcnt(0)
	v_pk_mul_f32 v[28:29], v[28:29], v[206:207]
	v_pk_mul_f32 v[30:31], v[30:31], v[20:21]
	global_store_dwordx4 v[144:145], v[28:31], off offset:-4096
	s_nop 0
	ds_read_b128 v[28:31], v246 offset:4096
	v_pk_mul_f32 v[20:21], v[24:25], v[116:117] op_sel_hi:[0,1]
	v_pk_mul_f32 v[206:207], v[24:25], v[96:97] op_sel_hi:[0,1]
	s_waitcnt lgkmcnt(0)
	v_pk_mul_f32 v[28:29], v[28:29], v[206:207]
	v_pk_mul_f32 v[30:31], v[30:31], v[20:21]
	global_store_dwordx4 v[144:145], v[28:31], off offset:-3072
	s_nop 0
	ds_read_b128 v[28:31], v246 offset:5120
	v_pk_mul_f32 v[20:21], v[24:25], v[114:115] op_sel_hi:[0,1]
	v_pk_mul_f32 v[206:207], v[24:25], v[94:95] op_sel_hi:[0,1]
	s_waitcnt lgkmcnt(0)
	v_pk_mul_f32 v[28:29], v[28:29], v[206:207]
	v_pk_mul_f32 v[30:31], v[30:31], v[20:21]
	global_store_dwordx4 v[144:145], v[28:31], off offset:-2048
	s_nop 0
	ds_read_b128 v[28:31], v246 offset:6144
	v_pk_mul_f32 v[20:21], v[24:25], v[112:113] op_sel_hi:[0,1]
	v_pk_mul_f32 v[206:207], v[24:25], v[92:93] op_sel_hi:[0,1]
	s_waitcnt lgkmcnt(0)
	v_pk_mul_f32 v[28:29], v[28:29], v[206:207]
	v_pk_mul_f32 v[30:31], v[30:31], v[20:21]
	global_store_dwordx4 v[144:145], v[28:31], off offset:-1024
	s_nop 0
	ds_read_b128 v[28:31], v246 offset:7168
	v_pk_mul_f32 v[20:21], v[24:25], v[110:111] op_sel_hi:[0,1]
	v_pk_mul_f32 v[24:25], v[24:25], v[90:91] op_sel_hi:[0,1]
	s_waitcnt lgkmcnt(0)
	v_pk_mul_f32 v[28:29], v[28:29], v[24:25]
	v_pk_mul_f32 v[30:31], v[30:31], v[20:21]
	global_store_dwordx4 v[144:145], v[28:31], off
	s_cbranch_vccnz .LBB0_2551
; __global__ void __launch_bounds__(NWAVES * 64, 2) fwd_kernel(Args a_unused) {
;     ...
;             if (more) { P12_SUM();
; #pragma unroll
;                 for (int j = 0; j < 8; ++j) v[j] = vn[j]; }
	v_cvt_f32_i32_sdwa v25, sext(v39) dst_sel:DWORD dst_unused:UNUSED_PAD src0_sel:BYTE_2
	v_cvt_f32_i32_sdwa v21, sext(v39) dst_sel:DWORD dst_unused:UNUSED_PAD src0_sel:BYTE_3
	v_cvt_f32_i32_sdwa v20, sext(v38) dst_sel:DWORD dst_unused:UNUSED_PAD src0_sel:BYTE_3
	v_cvt_f32_i32_sdwa v24, sext(v38) dst_sel:DWORD dst_unused:UNUSED_PAD src0_sel:BYTE_2
	v_mul_f32_e32 v28, v5, v25
	v_cvt_f32_i32_sdwa v25, sext(v55) dst_sel:DWORD dst_unused:UNUSED_PAD src0_sel:BYTE_2
	v_cvt_f32_i32_sdwa v29, sext(v54) dst_sel:DWORD dst_unused:UNUSED_PAD src0_sel:BYTE_2
	v_cvt_f32_i32_sdwa v71, sext(v38) dst_sel:DWORD dst_unused:UNUSED_PAD src0_sel:BYTE_1
	v_cvt_f32_i32_sdwa v70, sext(v38) dst_sel:DWORD dst_unused:UNUSED_PAD src0_sel:BYTE_0
	v_cvt_f32_i32_sdwa v73, sext(v39) dst_sel:DWORD dst_unused:UNUSED_PAD src0_sel:BYTE_1
	v_cvt_f32_i32_sdwa v72, sext(v39) dst_sel:DWORD dst_unused:UNUSED_PAD src0_sel:BYTE_0
	v_pk_mul_f32 v[20:21], v[4:5], v[20:21]
	v_cvt_f32_i32_sdwa v75, sext(v54) dst_sel:DWORD dst_unused:UNUSED_PAD src0_sel:BYTE_1
	v_cvt_f32_i32_sdwa v74, sext(v54) dst_sel:DWORD dst_unused:UNUSED_PAD src0_sel:BYTE_0
	v_mul_f32_e32 v24, v4, v24
	v_cvt_f32_i32_sdwa v77, sext(v55) dst_sel:DWORD dst_unused:UNUSED_PAD src0_sel:BYTE_3
	v_cvt_f32_i32_sdwa v76, sext(v54) dst_sel:DWORD dst_unused:UNUSED_PAD src0_sel:BYTE_3
	v_cvt_f32_i32_sdwa v79, sext(v55) dst_sel:DWORD dst_unused:UNUSED_PAD src0_sel:BYTE_1
	v_cvt_f32_i32_sdwa v78, sext(v55) dst_sel:DWORD dst_unused:UNUSED_PAD src0_sel:BYTE_0
	v_mul_f32_e32 v80, v17, v25
	v_mov_b32_e32 v25, v20
	v_mul_f32_e32 v30, v16, v29
	v_mov_b32_e32 v29, v21
	v_pk_add_f32 v[20:21], v[24:25], 0 op_sel_hi:[1,0]
	v_pk_fma_f32 v[24:25], v[4:5], v[70:71], 0 op_sel_hi:[0,1,0]
	v_pk_fma_f32 v[24:25], v[4:5], v[72:73], v[24:25] op_sel:[1,0,0]
	v_pk_mul_f32 v[76:77], v[16:17], v[76:77]
	v_pk_fma_f32 v[24:25], v[16:17], v[74:75], v[24:25] op_sel_hi:[0,1,1]
	v_pk_fma_f32 v[72:73], v[16:17], v[78:79], v[24:25] op_sel:[1,0,0]
	v_cvt_f32_i32_sdwa v25, sext(v41) dst_sel:DWORD dst_unused:UNUSED_PAD src0_sel:BYTE_2
	v_mov_b32_e32 v31, v76
	v_pk_add_f32 v[20:21], v[20:21], v[28:29]
	v_mov_b32_e32 v81, v77
	v_pk_add_f32 v[20:21], v[20:21], v[30:31]
	v_cvt_f32_i32_sdwa v24, sext(v40) dst_sel:DWORD dst_unused:UNUSED_PAD src0_sel:BYTE_2
	v_pk_add_f32 v[70:71], v[20:21], v[80:81]
	v_cvt_f32_i32_sdwa v21, sext(v41) dst_sel:DWORD dst_unused:UNUSED_PAD src0_sel:BYTE_3
	v_cvt_f32_i32_sdwa v20, sext(v40) dst_sel:DWORD dst_unused:UNUSED_PAD src0_sel:BYTE_3
	v_mul_f32_e32 v28, v27, v25
	v_cvt_f32_i32_sdwa v25, sext(v57) dst_sel:DWORD dst_unused:UNUSED_PAD src0_sel:BYTE_2
	v_cvt_f32_i32_sdwa v29, sext(v56) dst_sel:DWORD dst_unused:UNUSED_PAD src0_sel:BYTE_2
	v_cvt_f32_i32_sdwa v75, sext(v40) dst_sel:DWORD dst_unused:UNUSED_PAD src0_sel:BYTE_1
	v_cvt_f32_i32_sdwa v74, sext(v40) dst_sel:DWORD dst_unused:UNUSED_PAD src0_sel:BYTE_0
	v_cvt_f32_i32_sdwa v77, sext(v41) dst_sel:DWORD dst_unused:UNUSED_PAD src0_sel:BYTE_1
	v_cvt_f32_i32_sdwa v76, sext(v41) dst_sel:DWORD dst_unused:UNUSED_PAD src0_sel:BYTE_0
	v_pk_mul_f32 v[20:21], v[26:27], v[20:21]
	v_cvt_f32_i32_sdwa v79, sext(v56) dst_sel:DWORD dst_unused:UNUSED_PAD src0_sel:BYTE_1
	v_cvt_f32_i32_sdwa v78, sext(v56) dst_sel:DWORD dst_unused:UNUSED_PAD src0_sel:BYTE_0
	v_mul_f32_e32 v24, v26, v24
	v_cvt_f32_i32_sdwa v81, sext(v57) dst_sel:DWORD dst_unused:UNUSED_PAD src0_sel:BYTE_3
	v_cvt_f32_i32_sdwa v80, sext(v56) dst_sel:DWORD dst_unused:UNUSED_PAD src0_sel:BYTE_3
	v_cvt_f32_i32_sdwa v87, sext(v57) dst_sel:DWORD dst_unused:UNUSED_PAD src0_sel:BYTE_1
	v_cvt_f32_i32_sdwa v86, sext(v57) dst_sel:DWORD dst_unused:UNUSED_PAD src0_sel:BYTE_0
	v_mul_f32_e32 v88, v23, v25
	v_mov_b32_e32 v25, v20
	v_mul_f32_e32 v30, v22, v29
	v_mov_b32_e32 v29, v21
	v_pk_add_f32 v[20:21], v[24:25], 0 op_sel_hi:[1,0]
	v_pk_fma_f32 v[24:25], v[26:27], v[74:75], 0 op_sel_hi:[0,1,0]
	v_pk_fma_f32 v[24:25], v[26:27], v[76:77], v[24:25] op_sel:[1,0,0]
	v_pk_mul_f32 v[80:81], v[22:23], v[80:81]
	v_pk_fma_f32 v[24:25], v[22:23], v[78:79], v[24:25] op_sel_hi:[0,1,1]
	v_pk_fma_f32 v[76:77], v[22:23], v[86:87], v[24:25] op_sel:[1,0,0]
	v_cvt_f32_i32_sdwa v25, sext(v43) dst_sel:DWORD dst_unused:UNUSED_PAD src0_sel:BYTE_2
	v_mov_b32_e32 v31, v80
	v_pk_add_f32 v[20:21], v[20:21], v[28:29]
	v_mov_b32_e32 v89, v81
	v_pk_add_f32 v[20:21], v[20:21], v[30:31]
	v_cvt_f32_i32_sdwa v24, sext(v42) dst_sel:DWORD dst_unused:UNUSED_PAD src0_sel:BYTE_2
	v_pk_add_f32 v[74:75], v[20:21], v[88:89]
	v_cvt_f32_i32_sdwa v21, sext(v43) dst_sel:DWORD dst_unused:UNUSED_PAD src0_sel:BYTE_3
	v_cvt_f32_i32_sdwa v20, sext(v42) dst_sel:DWORD dst_unused:UNUSED_PAD src0_sel:BYTE_3
	v_mul_f32_e32 v28, v7, v25
	v_cvt_f32_i32_sdwa v25, sext(v59) dst_sel:DWORD dst_unused:UNUSED_PAD src0_sel:BYTE_2
	v_cvt_f32_i32_sdwa v29, sext(v58) dst_sel:DWORD dst_unused:UNUSED_PAD src0_sel:BYTE_2
	v_cvt_f32_i32_sdwa v79, sext(v42) dst_sel:DWORD dst_unused:UNUSED_PAD src0_sel:BYTE_1
	v_cvt_f32_i32_sdwa v78, sext(v42) dst_sel:DWORD dst_unused:UNUSED_PAD src0_sel:BYTE_0
	v_cvt_f32_i32_sdwa v81, sext(v43) dst_sel:DWORD dst_unused:UNUSED_PAD src0_sel:BYTE_1
	v_cvt_f32_i32_sdwa v80, sext(v43) dst_sel:DWORD dst_unused:UNUSED_PAD src0_sel:BYTE_0
	v_pk_mul_f32 v[20:21], v[6:7], v[20:21]
	v_cvt_f32_i32_sdwa v87, sext(v58) dst_sel:DWORD dst_unused:UNUSED_PAD src0_sel:BYTE_1
	v_cvt_f32_i32_sdwa v86, sext(v58) dst_sel:DWORD dst_unused:UNUSED_PAD src0_sel:BYTE_0
	v_mul_f32_e32 v24, v6, v24
	v_cvt_f32_i32_sdwa v89, sext(v59) dst_sel:DWORD dst_unused:UNUSED_PAD src0_sel:BYTE_3
	v_cvt_f32_i32_sdwa v88, sext(v58) dst_sel:DWORD dst_unused:UNUSED_PAD src0_sel:BYTE_3
	v_cvt_f32_i32_sdwa v91, sext(v59) dst_sel:DWORD dst_unused:UNUSED_PAD src0_sel:BYTE_1
	v_cvt_f32_i32_sdwa v90, sext(v59) dst_sel:DWORD dst_unused:UNUSED_PAD src0_sel:BYTE_0
	v_mul_f32_e32 v92, v19, v25
	v_mov_b32_e32 v25, v20
	v_mul_f32_e32 v30, v18, v29
	v_mov_b32_e32 v29, v21
	v_pk_add_f32 v[20:21], v[24:25], 0 op_sel_hi:[1,0]
	v_pk_fma_f32 v[24:25], v[6:7], v[78:79], 0 op_sel_hi:[0,1,0]
	v_pk_fma_f32 v[24:25], v[6:7], v[80:81], v[24:25] op_sel:[1,0,0]
	v_pk_mul_f32 v[88:89], v[18:19], v[88:89]
	v_pk_fma_f32 v[24:25], v[18:19], v[86:87], v[24:25] op_sel_hi:[0,1,1]
	v_pk_fma_f32 v[80:81], v[18:19], v[90:91], v[24:25] op_sel:[1,0,0]
	v_cvt_f32_i32_sdwa v25, sext(v45) dst_sel:DWORD dst_unused:UNUSED_PAD src0_sel:BYTE_2
	v_mov_b32_e32 v31, v88
	v_pk_add_f32 v[20:21], v[20:21], v[28:29]
	v_mov_b32_e32 v93, v89
	v_pk_add_f32 v[20:21], v[20:21], v[30:31]
	v_cvt_f32_i32_sdwa v24, sext(v44) dst_sel:DWORD dst_unused:UNUSED_PAD src0_sel:BYTE_2
	v_pk_add_f32 v[78:79], v[20:21], v[92:93]
	v_cvt_f32_i32_sdwa v21, sext(v45) dst_sel:DWORD dst_unused:UNUSED_PAD src0_sel:BYTE_3
	v_cvt_f32_i32_sdwa v20, sext(v44) dst_sel:DWORD dst_unused:UNUSED_PAD src0_sel:BYTE_3
	v_mul_f32_e32 v28, v159, v25
	v_cvt_f32_i32_sdwa v25, sext(v61) dst_sel:DWORD dst_unused:UNUSED_PAD src0_sel:BYTE_2
	v_cvt_f32_i32_sdwa v29, sext(v60) dst_sel:DWORD dst_unused:UNUSED_PAD src0_sel:BYTE_2
	v_cvt_f32_i32_sdwa v87, sext(v44) dst_sel:DWORD dst_unused:UNUSED_PAD src0_sel:BYTE_1
	v_cvt_f32_i32_sdwa v86, sext(v44) dst_sel:DWORD dst_unused:UNUSED_PAD src0_sel:BYTE_0
	v_cvt_f32_i32_sdwa v89, sext(v45) dst_sel:DWORD dst_unused:UNUSED_PAD src0_sel:BYTE_1
	v_cvt_f32_i32_sdwa v88, sext(v45) dst_sel:DWORD dst_unused:UNUSED_PAD src0_sel:BYTE_0
	v_pk_mul_f32 v[20:21], v[158:159], v[20:21]
	v_cvt_f32_i32_sdwa v91, sext(v60) dst_sel:DWORD dst_unused:UNUSED_PAD src0_sel:BYTE_1
	v_cvt_f32_i32_sdwa v90, sext(v60) dst_sel:DWORD dst_unused:UNUSED_PAD src0_sel:BYTE_0
	v_mul_f32_e32 v24, v158, v24
	v_cvt_f32_i32_sdwa v93, sext(v61) dst_sel:DWORD dst_unused:UNUSED_PAD src0_sel:BYTE_3
	v_cvt_f32_i32_sdwa v92, sext(v60) dst_sel:DWORD dst_unused:UNUSED_PAD src0_sel:BYTE_3
	v_cvt_f32_i32_sdwa v95, sext(v61) dst_sel:DWORD dst_unused:UNUSED_PAD src0_sel:BYTE_1
	v_cvt_f32_i32_sdwa v94, sext(v61) dst_sel:DWORD dst_unused:UNUSED_PAD src0_sel:BYTE_0
	v_mul_f32_e32 v96, v33, v25
	v_mov_b32_e32 v25, v20
	v_mul_f32_e32 v30, v32, v29
	v_mov_b32_e32 v29, v21
	v_pk_add_f32 v[20:21], v[24:25], 0 op_sel_hi:[1,0]
	v_pk_fma_f32 v[24:25], v[158:159], v[86:87], 0 op_sel_hi:[0,1,0]
	v_pk_fma_f32 v[24:25], v[158:159], v[88:89], v[24:25] op_sel:[1,0,0]
	v_pk_mul_f32 v[92:93], v[32:33], v[92:93]
	v_pk_fma_f32 v[24:25], v[32:33], v[90:91], v[24:25] op_sel_hi:[0,1,1]
	v_pk_fma_f32 v[88:89], v[32:33], v[94:95], v[24:25] op_sel:[1,0,0]
	v_cvt_f32_i32_sdwa v25, sext(v47) dst_sel:DWORD dst_unused:UNUSED_PAD src0_sel:BYTE_2
	v_mov_b32_e32 v31, v92
	v_pk_add_f32 v[20:21], v[20:21], v[28:29]
	v_mov_b32_e32 v97, v93
	v_pk_add_f32 v[20:21], v[20:21], v[30:31]
	v_cvt_f32_i32_sdwa v24, sext(v46) dst_sel:DWORD dst_unused:UNUSED_PAD src0_sel:BYTE_2
	v_pk_add_f32 v[86:87], v[20:21], v[96:97]
	v_cvt_f32_i32_sdwa v21, sext(v47) dst_sel:DWORD dst_unused:UNUSED_PAD src0_sel:BYTE_3
	v_cvt_f32_i32_sdwa v20, sext(v46) dst_sel:DWORD dst_unused:UNUSED_PAD src0_sel:BYTE_3
	v_mul_f32_e32 v28, v1, v25
	v_cvt_f32_i32_sdwa v25, sext(v63) dst_sel:DWORD dst_unused:UNUSED_PAD src0_sel:BYTE_2
	v_cvt_f32_i32_sdwa v29, sext(v62) dst_sel:DWORD dst_unused:UNUSED_PAD src0_sel:BYTE_2
	v_cvt_f32_i32_sdwa v91, sext(v46) dst_sel:DWORD dst_unused:UNUSED_PAD src0_sel:BYTE_1
	v_cvt_f32_i32_sdwa v90, sext(v46) dst_sel:DWORD dst_unused:UNUSED_PAD src0_sel:BYTE_0
	v_cvt_f32_i32_sdwa v93, sext(v47) dst_sel:DWORD dst_unused:UNUSED_PAD src0_sel:BYTE_1
	v_cvt_f32_i32_sdwa v92, sext(v47) dst_sel:DWORD dst_unused:UNUSED_PAD src0_sel:BYTE_0
	v_pk_mul_f32 v[20:21], v[0:1], v[20:21]
	v_cvt_f32_i32_sdwa v95, sext(v62) dst_sel:DWORD dst_unused:UNUSED_PAD src0_sel:BYTE_1
	v_cvt_f32_i32_sdwa v94, sext(v62) dst_sel:DWORD dst_unused:UNUSED_PAD src0_sel:BYTE_0
	v_mul_f32_e32 v24, v0, v24
	v_cvt_f32_i32_sdwa v97, sext(v63) dst_sel:DWORD dst_unused:UNUSED_PAD src0_sel:BYTE_3
	v_cvt_f32_i32_sdwa v96, sext(v62) dst_sel:DWORD dst_unused:UNUSED_PAD src0_sel:BYTE_3
	v_cvt_f32_i32_sdwa v99, sext(v63) dst_sel:DWORD dst_unused:UNUSED_PAD src0_sel:BYTE_1
	v_cvt_f32_i32_sdwa v98, sext(v63) dst_sel:DWORD dst_unused:UNUSED_PAD src0_sel:BYTE_0
	v_mul_f32_e32 v100, v13, v25
	v_mov_b32_e32 v25, v20
	v_mul_f32_e32 v30, v12, v29
	v_mov_b32_e32 v29, v21
	v_pk_add_f32 v[20:21], v[24:25], 0 op_sel_hi:[1,0]
	v_pk_fma_f32 v[24:25], v[0:1], v[90:91], 0 op_sel_hi:[0,1,0]
	v_pk_fma_f32 v[24:25], v[0:1], v[92:93], v[24:25] op_sel:[1,0,0]
	v_pk_mul_f32 v[96:97], v[12:13], v[96:97]
	v_pk_fma_f32 v[24:25], v[12:13], v[94:95], v[24:25] op_sel_hi:[0,1,1]
	v_pk_fma_f32 v[142:143], v[12:13], v[98:99], v[24:25] op_sel:[1,0,0]
	v_cvt_f32_i32_sdwa v25, sext(v49) dst_sel:DWORD dst_unused:UNUSED_PAD src0_sel:BYTE_2
	v_mov_b32_e32 v31, v96
	v_pk_add_f32 v[20:21], v[20:21], v[28:29]
	v_mov_b32_e32 v101, v97
	v_pk_add_f32 v[20:21], v[20:21], v[30:31]
	v_cvt_f32_i32_sdwa v24, sext(v48) dst_sel:DWORD dst_unused:UNUSED_PAD src0_sel:BYTE_2
	v_pk_add_f32 v[140:141], v[20:21], v[100:101]
	v_cvt_f32_i32_sdwa v21, sext(v49) dst_sel:DWORD dst_unused:UNUSED_PAD src0_sel:BYTE_3
	v_cvt_f32_i32_sdwa v20, sext(v48) dst_sel:DWORD dst_unused:UNUSED_PAD src0_sel:BYTE_3
	v_mul_f32_e32 v28, v157, v25
	v_cvt_f32_i32_sdwa v25, sext(v65) dst_sel:DWORD dst_unused:UNUSED_PAD src0_sel:BYTE_2
	v_cvt_f32_i32_sdwa v29, sext(v64) dst_sel:DWORD dst_unused:UNUSED_PAD src0_sel:BYTE_2
	v_cvt_f32_i32_sdwa v91, sext(v48) dst_sel:DWORD dst_unused:UNUSED_PAD src0_sel:BYTE_1
; __global__ void __launch_bounds__(NWAVES * 64, 2) fwd_kernel(Args a_unused) {
;     ...
;             if (more) { P12_SUM();
; #pragma unroll
;                 for (int j = 0; j < 8; ++j) v[j] = vn[j]; }
	v_cvt_f32_i32_sdwa v90, sext(v48) dst_sel:DWORD dst_unused:UNUSED_PAD src0_sel:BYTE_0
	v_cvt_f32_i32_sdwa v93, sext(v49) dst_sel:DWORD dst_unused:UNUSED_PAD src0_sel:BYTE_1
	v_cvt_f32_i32_sdwa v92, sext(v49) dst_sel:DWORD dst_unused:UNUSED_PAD src0_sel:BYTE_0
	v_pk_mul_f32 v[20:21], v[156:157], v[20:21]
	v_cvt_f32_i32_sdwa v95, sext(v64) dst_sel:DWORD dst_unused:UNUSED_PAD src0_sel:BYTE_1
	v_cvt_f32_i32_sdwa v94, sext(v64) dst_sel:DWORD dst_unused:UNUSED_PAD src0_sel:BYTE_0
	v_mul_f32_e32 v24, v156, v24
	v_cvt_f32_i32_sdwa v97, sext(v65) dst_sel:DWORD dst_unused:UNUSED_PAD src0_sel:BYTE_3
	v_cvt_f32_i32_sdwa v96, sext(v64) dst_sel:DWORD dst_unused:UNUSED_PAD src0_sel:BYTE_3
	v_cvt_f32_i32_sdwa v99, sext(v65) dst_sel:DWORD dst_unused:UNUSED_PAD src0_sel:BYTE_1
	v_cvt_f32_i32_sdwa v98, sext(v65) dst_sel:DWORD dst_unused:UNUSED_PAD src0_sel:BYTE_0
	v_mul_f32_e32 v100, v35, v25
	v_mov_b32_e32 v25, v20
	v_mul_f32_e32 v30, v34, v29
	v_mov_b32_e32 v29, v21
	v_pk_add_f32 v[20:21], v[24:25], 0 op_sel_hi:[1,0]
	v_pk_fma_f32 v[24:25], v[156:157], v[90:91], 0 op_sel_hi:[0,1,0]
	v_pk_fma_f32 v[24:25], v[156:157], v[92:93], v[24:25] op_sel:[1,0,0]
	v_pk_mul_f32 v[96:97], v[34:35], v[96:97]
	v_pk_fma_f32 v[24:25], v[34:35], v[94:95], v[24:25] op_sel_hi:[0,1,1]
	v_pk_fma_f32 v[154:155], v[34:35], v[98:99], v[24:25] op_sel:[1,0,0]
	v_cvt_f32_i32_sdwa v25, sext(v51) dst_sel:DWORD dst_unused:UNUSED_PAD src0_sel:BYTE_2
	v_mov_b32_e32 v31, v96
	v_pk_add_f32 v[20:21], v[20:21], v[28:29]
	v_mov_b32_e32 v101, v97
	v_pk_add_f32 v[20:21], v[20:21], v[30:31]
	v_cvt_f32_i32_sdwa v24, sext(v50) dst_sel:DWORD dst_unused:UNUSED_PAD src0_sel:BYTE_2
	v_pk_add_f32 v[152:153], v[20:21], v[100:101]
	v_cvt_f32_i32_sdwa v21, sext(v51) dst_sel:DWORD dst_unused:UNUSED_PAD src0_sel:BYTE_3
	v_cvt_f32_i32_sdwa v20, sext(v50) dst_sel:DWORD dst_unused:UNUSED_PAD src0_sel:BYTE_3
	v_mul_f32_e32 v28, v3, v25
	v_cvt_f32_i32_sdwa v25, sext(v67) dst_sel:DWORD dst_unused:UNUSED_PAD src0_sel:BYTE_2
	v_cvt_f32_i32_sdwa v29, sext(v66) dst_sel:DWORD dst_unused:UNUSED_PAD src0_sel:BYTE_2
	v_cvt_f32_i32_sdwa v91, sext(v50) dst_sel:DWORD dst_unused:UNUSED_PAD src0_sel:BYTE_1
	v_cvt_f32_i32_sdwa v90, sext(v50) dst_sel:DWORD dst_unused:UNUSED_PAD src0_sel:BYTE_0
	v_cvt_f32_i32_sdwa v93, sext(v51) dst_sel:DWORD dst_unused:UNUSED_PAD src0_sel:BYTE_1
	v_cvt_f32_i32_sdwa v92, sext(v51) dst_sel:DWORD dst_unused:UNUSED_PAD src0_sel:BYTE_0
	v_pk_mul_f32 v[20:21], v[2:3], v[20:21]
	v_cvt_f32_i32_sdwa v95, sext(v66) dst_sel:DWORD dst_unused:UNUSED_PAD src0_sel:BYTE_1
	v_cvt_f32_i32_sdwa v94, sext(v66) dst_sel:DWORD dst_unused:UNUSED_PAD src0_sel:BYTE_0
	v_mul_f32_e32 v24, v2, v24
	v_cvt_f32_i32_sdwa v97, sext(v67) dst_sel:DWORD dst_unused:UNUSED_PAD src0_sel:BYTE_3
	v_cvt_f32_i32_sdwa v96, sext(v66) dst_sel:DWORD dst_unused:UNUSED_PAD src0_sel:BYTE_3
	v_cvt_f32_i32_sdwa v99, sext(v67) dst_sel:DWORD dst_unused:UNUSED_PAD src0_sel:BYTE_1
	v_cvt_f32_i32_sdwa v98, sext(v67) dst_sel:DWORD dst_unused:UNUSED_PAD src0_sel:BYTE_0
	v_mul_f32_e32 v100, v15, v25
	v_mov_b32_e32 v25, v20
	v_mul_f32_e32 v30, v14, v29
	v_mov_b32_e32 v29, v21
	v_pk_add_f32 v[20:21], v[24:25], 0 op_sel_hi:[1,0]
	v_pk_fma_f32 v[24:25], v[2:3], v[90:91], 0 op_sel_hi:[0,1,0]
	v_pk_fma_f32 v[24:25], v[2:3], v[92:93], v[24:25] op_sel:[1,0,0]
	v_pk_mul_f32 v[96:97], v[14:15], v[96:97]
	v_pk_fma_f32 v[24:25], v[14:15], v[94:95], v[24:25] op_sel_hi:[0,1,1]
	v_pk_fma_f32 v[166:167], v[14:15], v[98:99], v[24:25] op_sel:[1,0,0]
	v_cvt_f32_i32_sdwa v25, sext(v53) dst_sel:DWORD dst_unused:UNUSED_PAD src0_sel:BYTE_2
	v_mov_b32_e32 v31, v96
	v_pk_add_f32 v[20:21], v[20:21], v[28:29]
	v_mov_b32_e32 v101, v97
	v_pk_add_f32 v[20:21], v[20:21], v[30:31]
	v_cvt_f32_i32_sdwa v24, sext(v52) dst_sel:DWORD dst_unused:UNUSED_PAD src0_sel:BYTE_2
	v_pk_add_f32 v[160:161], v[20:21], v[100:101]
	v_cvt_f32_i32_sdwa v21, sext(v53) dst_sel:DWORD dst_unused:UNUSED_PAD src0_sel:BYTE_3
	v_cvt_f32_i32_sdwa v20, sext(v52) dst_sel:DWORD dst_unused:UNUSED_PAD src0_sel:BYTE_3
	v_mul_f32_e32 v28, v151, v25
	v_cvt_f32_i32_sdwa v25, sext(v69) dst_sel:DWORD dst_unused:UNUSED_PAD src0_sel:BYTE_2
	v_cvt_f32_i32_sdwa v29, sext(v68) dst_sel:DWORD dst_unused:UNUSED_PAD src0_sel:BYTE_2
	v_cvt_f32_i32_sdwa v91, sext(v52) dst_sel:DWORD dst_unused:UNUSED_PAD src0_sel:BYTE_1
	v_cvt_f32_i32_sdwa v90, sext(v52) dst_sel:DWORD dst_unused:UNUSED_PAD src0_sel:BYTE_0
	v_cvt_f32_i32_sdwa v97, sext(v69) dst_sel:DWORD dst_unused:UNUSED_PAD src0_sel:BYTE_3
	v_cvt_f32_i32_sdwa v96, sext(v68) dst_sel:DWORD dst_unused:UNUSED_PAD src0_sel:BYTE_3
	v_cvt_f32_i32_sdwa v93, sext(v53) dst_sel:DWORD dst_unused:UNUSED_PAD src0_sel:BYTE_1
	v_cvt_f32_i32_sdwa v92, sext(v53) dst_sel:DWORD dst_unused:UNUSED_PAD src0_sel:BYTE_0
	v_pk_mul_f32 v[20:21], v[150:151], v[20:21]
	v_cvt_f32_i32_sdwa v95, sext(v68) dst_sel:DWORD dst_unused:UNUSED_PAD src0_sel:BYTE_1
	v_cvt_f32_i32_sdwa v94, sext(v68) dst_sel:DWORD dst_unused:UNUSED_PAD src0_sel:BYTE_0
	v_mul_f32_e32 v24, v150, v24
	v_cvt_f32_i32_sdwa v99, sext(v69) dst_sel:DWORD dst_unused:UNUSED_PAD src0_sel:BYTE_1
	v_cvt_f32_i32_sdwa v98, sext(v69) dst_sel:DWORD dst_unused:UNUSED_PAD src0_sel:BYTE_0
	v_mul_f32_e32 v100, v149, v25
	v_mov_b32_e32 v25, v20
	v_mul_f32_e32 v30, v148, v29
	v_pk_mul_f32 v[96:97], v[148:149], v[96:97]
	v_mov_b32_e32 v29, v21
	v_pk_add_f32 v[20:21], v[24:25], 0 op_sel_hi:[1,0]
	v_pk_fma_f32 v[24:25], v[150:151], v[90:91], 0 op_sel_hi:[0,1,0]
	v_mov_b32_e32 v31, v96
	v_pk_add_f32 v[20:21], v[20:21], v[28:29]
	v_pk_fma_f32 v[24:25], v[150:151], v[92:93], v[24:25] op_sel:[1,0,0]
	v_mov_b32_e32 v101, v97
	v_pk_add_f32 v[20:21], v[20:21], v[30:31]
	v_pk_fma_f32 v[24:25], v[148:149], v[94:95], v[24:25] op_sel_hi:[0,1,1]
	v_pk_add_f32 v[168:169], v[20:21], v[100:101]
	v_pk_fma_f32 v[170:171], v[148:149], v[98:99], v[24:25] op_sel:[1,0,0]
	v_mov_b32_e32 v90, v162
	v_mov_b32_e32 v91, v175
	v_mov_b32_e32 v110, v190
	v_mov_b32_e32 v111, v198
	v_mov_b32_e32 v92, v163
	v_mov_b32_e32 v93, v183
	v_mov_b32_e32 v112, v191
	v_mov_b32_e32 v113, v199
	v_mov_b32_e32 v94, v164
	v_mov_b32_e32 v95, v184
	v_mov_b32_e32 v114, v192
	v_mov_b32_e32 v115, v200
	v_mov_b32_e32 v96, v165
	v_mov_b32_e32 v97, v185
	v_mov_b32_e32 v116, v193
	v_mov_b32_e32 v117, v201
	v_mov_b32_e32 v98, v172
	v_mov_b32_e32 v99, v186
	v_mov_b32_e32 v118, v194
	v_mov_b32_e32 v119, v202
	v_mov_b32_e32 v100, v173
	v_mov_b32_e32 v101, v187
	v_mov_b32_e32 v120, v195
	v_mov_b32_e32 v121, v203
	v_mov_b32_e32 v102, v174
	v_mov_b32_e32 v103, v188
	v_mov_b32_e32 v122, v196
	v_mov_b32_e32 v123, v204
	v_mov_b32_e32 v104, v182
	v_mov_b32_e32 v105, v189
	v_mov_b32_e32 v124, v197
	v_mov_b32_e32 v125, v205
	s_branch .LBB0_2551
